# MoE up/down bodies: one static s_setprio 1 for the staggered half (waves 4-7)
# baseline (speedup 1.0000x reference)
; #define MU_GLDS_A(buf, kt) do { _Pragma("unroll") for (int i = 0; i < NMU; ++i) \
;         __builtin_amdgcn_global_load_lds((const unsigned*)((const char*)A + aoff[i] + (size_t)(kt) * 128), (PG8_LAS unsigned*)(MU_SA(buf) + wid * 1024 + i * 8192), 16, 0, 0); } while (0)
; #define MU_B_ISSUE(sb, kt) do { const char* kb_ = Bb + (size_t)(kt) * (64 * (size_t)RB); _Pragma("unroll") for (int j = 0; j < 8; ++j) { const char* p_ = kb_ + (size_t)j * RB; \
;         asm volatile("global_load_dwordx2 %0, %1, off" : "=&v"(sb[j]) : "v"(p_) : "memory"); } } while (0)
; #define MU_B_WAIT(sb, N) asm volatile("s_waitcnt vmcnt(%8)" : "+v"(sb[0]), "+v"(sb[1]), "+v"(sb[2]), "+v"(sb[3]), "+v"(sb[4]), "+v"(sb[5]), "+v"(sb[6]), "+v"(sb[7]) : "n"(N) : "memory")
; #define MU_COMPUTE(buf) MU_COMPUTE_N(buf, NMU)
; template <int MODE>
; __device__ __forceinline__ void moe_unit(PG8_LAS unsigned char* lds, int e, int cb, int slot0  , int nv  , const bf16_t* A, const int* slot_tok,
;                                          const float* W0, const float* W1, bf16_t* OUT, const float* slot_rs  , const int* slot_dst) {
;     ...
;     f32x4 acc[NMU][4];
; #pragma unroll
;     for (int m = 0; m < NMU; ++m)
; #pragma unroll
;         for (int n = 0; n < 4; ++n) acc[m][n] = (f32x4){0.f, 0.f, 0.f, 0.f};
;     f32x2 s0[8], s1[8];
;     float g0[8];
;     MU_GLDS_A(0, 0); MU_B_ISSUE(s0, 0); MU_G_LOAD(g0, 0); MU_B_ISSUE(s1, 1);
;     MU_B_WAIT(s0, 8); MU_B_WRITE(s0, 0, g0); __builtin_amdgcn_sched_barrier(0); MU_B_ISSUE(s0, 2);
;     asm volatile("s_waitcnt vmcnt(16)" ::: "memory");
;     asm volatile("s_waitcnt lgkmcnt(0)" ::: "memory"); __builtin_amdgcn_s_barrier(); asm volatile("" ::: "memory");
; #pragma unroll 1
;     for (int t = 0; t < nt; t += 2) {
;         if (t + 2 < nt) MU_B_WAIT(s1, 8); else MU_B_WAIT(s1, 0);
;         MU_G_LOAD(g0, t + 1); MU_B_WRITE(s1, 1, g0); __builtin_amdgcn_sched_barrier(0); MU_GLDS_A(1, t + 1); __builtin_amdgcn_sched_barrier(0);
;         if (t + 3 < nt) { MU_B_ISSUE(s1, t + 3); }
;         MU_COMPUTE(0);
;         MU_END(t + 3 >= nt);
;         if (t + 2 < nt) { MU_B_WAIT(s0, 8); MU_G_LOAD(g0, t + 2); MU_B_WRITE(s0, 0, g0); __builtin_amdgcn_sched_barrier(0); MU_GLDS_A(0, t + 2); __builtin_amdgcn_sched_barrier(0); }
;         if (t + 4 < nt) { MU_B_ISSUE(s0, t + 4); }
;         MU_COMPUTE(1);
;         MU_END(t + 4 >= nt);
.Lmu_grpY4:
	s_setprio 1
	s_add_i32 s47, s44, s6
	s_add_u32 s30, s30, 0x80
	s_addc_u32 s31, s31, 0
	s_mov_b32 m0, s47
	s_nop 0
	global_load_lds_dwordx4 v86, s[30:31]
	s_add_i32 m0, s47, 0x2000
	s_nop 0
	global_load_lds_dwordx4 v134, s[30:31]
	s_add_i32 m0, s47, 0x4000
	s_nop 0
	global_load_lds_dwordx4 v136, s[30:31]
	s_add_i32 m0, s47, 0x6000
	s_nop 0
	global_load_lds_dwordx4 v138, s[30:31]
	s_add_i32 m0, s47, 0x8000
	s_nop 0
	global_load_lds_dwordx4 v140, s[30:31]
	s_waitcnt vmcnt(29)
	v_mul_f32_e32 v114, s20, v114
	v_mul_f32_e32 v115, s20, v115
	v_mul_f32_e32 v116, s21, v116
	v_mul_f32_e32 v117, s21, v117
	v_mul_f32_e32 v118, s22, v118
	v_mul_f32_e32 v119, s22, v119
	v_mul_f32_e32 v120, s23, v120
	v_mul_f32_e32 v121, s23, v121
	v_mul_f32_e32 v122, s24, v122
	v_mul_f32_e32 v123, s24, v123
	v_mul_f32_e32 v124, s25, v124
	v_mul_f32_e32 v125, s25, v125
	v_mul_f32_e32 v126, s26, v126
	v_mul_f32_e32 v127, s26, v127
	v_mul_f32_e32 v128, s27, v128
	v_mul_f32_e32 v129, s27, v129
	v_cvt_pk_bf16_f32 v158, v114, v116
	v_cvt_pk_bf16_f32 v159, v118, v120
	v_cvt_pk_bf16_f32 v160, v122, v124
	v_cvt_pk_bf16_f32 v161, v126, v128
	v_cvt_pk_bf16_f32 v162, v115, v117
	v_cvt_pk_bf16_f32 v163, v119, v121
	v_cvt_pk_bf16_f32 v164, v123, v125
	v_cvt_pk_bf16_f32 v165, v127, v129
	ds_write_b128 v1, v[158:161] offset:19456
	ds_write_b128 v1, v[162:165] offset:19584
	v_add_u32_e32 v91, s42, v135
	v_add_u32_e32 v93, s42, v137
	ds_read_b128 v[238:241], v139 offset:0
	ds_read_b128 v[242:245], v139 offset:2048
	ds_read_b128 v[246:249], v139 offset:4096
	ds_read_b128 v[250:253], v139 offset:6144
	ds_read_b128 v[218:221], v91 offset:0
	ds_read_b128 v[222:225], v91 offset:2048
	ds_read_b128 v[226:229], v91 offset:4096
	ds_read_b128 v[230:233], v91 offset:6144
	s_waitcnt lgkmcnt(0)
	s_load_dwordx8 s[12:19], s[28:29], 0x0
	s_add_u32 s28, s28, 0x100
	s_addc_u32 s29, s29, 0
	v_mfma_f32_16x16x32_bf16 v[78:81], v[238:241], v[218:221], v[78:81]
	v_mfma_f32_16x16x32_bf16 v[74:77], v[242:245], v[218:221], v[74:77]
	v_mfma_f32_16x16x32_bf16 v[70:73], v[246:249], v[218:221], v[70:73]
	v_mfma_f32_16x16x32_bf16 v[66:69], v[250:253], v[218:221], v[66:69]
	ds_read_b128 v[218:221], v93 offset:0
	ds_read_b128 v[142:145], v141 offset:0
	v_lshl_add_u64 v[132:133], v[132:133], 0, s[40:41]
	global_load_dwordx2 v[114:115], v[132:133], off
	global_load_dwordx2 v[116:117], v[132:133], off offset:2048
	v_mfma_f32_16x16x32_bf16 v[62:65], v[238:241], v[222:225], v[62:65]
	v_mfma_f32_16x16x32_bf16 v[58:61], v[242:245], v[222:225], v[58:61]
	v_mfma_f32_16x16x32_bf16 v[54:57], v[246:249], v[222:225], v[54:57]
	v_mfma_f32_16x16x32_bf16 v[50:53], v[250:253], v[222:225], v[50:53]
	ds_read_b128 v[222:225], v93 offset:2048
	ds_read_b128 v[146:149], v141 offset:2048
	v_lshl_add_u64 v[166:167], v[132:133], 0, s[34:35]
	global_load_dwordx2 v[118:119], v[166:167], off
	global_load_dwordx2 v[120:121], v[166:167], off offset:2048
	v_mfma_f32_16x16x32_bf16 v[46:49], v[238:241], v[226:229], v[46:49]
	v_mfma_f32_16x16x32_bf16 v[42:45], v[242:245], v[226:229], v[42:45]
	v_mfma_f32_16x16x32_bf16 v[38:41], v[246:249], v[226:229], v[38:41]
	v_mfma_f32_16x16x32_bf16 v[34:37], v[250:253], v[226:229], v[34:37]
	ds_read_b128 v[226:229], v93 offset:4096
	ds_read_b128 v[150:153], v141 offset:4096
	v_lshl_add_u64 v[166:167], v[132:133], 0, s[36:37]
	global_load_dwordx2 v[122:123], v[166:167], off
	global_load_dwordx2 v[124:125], v[166:167], off offset:2048
	v_mfma_f32_16x16x32_bf16 v[18:21], v[238:241], v[230:233], v[18:21]
	v_mfma_f32_16x16x32_bf16 v[22:25], v[242:245], v[230:233], v[22:25]
	v_mfma_f32_16x16x32_bf16 v[26:29], v[246:249], v[230:233], v[26:29]
	v_mfma_f32_16x16x32_bf16 v[30:33], v[250:253], v[230:233], v[30:33]
	ds_read_b128 v[230:233], v93 offset:6144
	ds_read_b128 v[154:157], v141 offset:6144
	v_lshl_add_u64 v[166:167], v[132:133], 0, s[38:39]
	global_load_dwordx2 v[126:127], v[166:167], off
	global_load_dwordx2 v[128:129], v[166:167], off offset:2048
	s_waitcnt lgkmcnt(0)
	s_barrier
	s_mov_b32 s47, s42
	s_mov_b32 s42, s43
	s_mov_b32 s43, s44
	s_mov_b32 s44, s47
	s_add_i32 s47, s44, s6
	s_add_u32 s30, s30, 0x80
	s_addc_u32 s31, s31, 0
	v_mfma_f32_16x16x32_bf16 v[78:81], v[142:145], v[218:221], v[78:81]
	v_mfma_f32_16x16x32_bf16 v[74:77], v[146:149], v[218:221], v[74:77]
	v_mfma_f32_16x16x32_bf16 v[70:73], v[150:153], v[218:221], v[70:73]
	v_mfma_f32_16x16x32_bf16 v[66:69], v[154:157], v[218:221], v[66:69]
	s_mov_b32 m0, s47
	s_nop 0
	global_load_lds_dwordx4 v86, s[30:31]
	v_mfma_f32_16x16x32_bf16 v[62:65], v[142:145], v[222:225], v[62:65]
	v_mfma_f32_16x16x32_bf16 v[58:61], v[146:149], v[222:225], v[58:61]
	v_mfma_f32_16x16x32_bf16 v[54:57], v[150:153], v[222:225], v[54:57]
	v_mfma_f32_16x16x32_bf16 v[50:53], v[154:157], v[222:225], v[50:53]
	s_add_i32 m0, s47, 0x2000
	s_nop 0
	global_load_lds_dwordx4 v134, s[30:31]
	v_mfma_f32_16x16x32_bf16 v[46:49], v[142:145], v[226:229], v[46:49]
	v_mfma_f32_16x16x32_bf16 v[42:45], v[146:149], v[226:229], v[42:45]
	v_mfma_f32_16x16x32_bf16 v[38:41], v[150:153], v[226:229], v[38:41]
	v_mfma_f32_16x16x32_bf16 v[34:37], v[154:157], v[226:229], v[34:37]
	s_add_i32 m0, s47, 0x4000
	s_nop 0
	global_load_lds_dwordx4 v136, s[30:31]
	v_mfma_f32_16x16x32_bf16 v[18:21], v[142:145], v[230:233], v[18:21]
	v_mfma_f32_16x16x32_bf16 v[22:25], v[146:149], v[230:233], v[22:25]
	v_mfma_f32_16x16x32_bf16 v[26:29], v[150:153], v[230:233], v[26:29]
	v_mfma_f32_16x16x32_bf16 v[30:33], v[154:157], v[230:233], v[30:33]
	s_add_i32 m0, s47, 0x6000
	s_nop 0
	global_load_lds_dwordx4 v138, s[30:31]
	s_add_i32 m0, s47, 0x8000
	s_nop 0
	global_load_lds_dwordx4 v140, s[30:31]
	s_waitcnt vmcnt(34)
; #define MU_GLDS_A(buf, kt) do { _Pragma("unroll") for (int i = 0; i < NMU; ++i) \
;         __builtin_amdgcn_global_load_lds((const unsigned*)((const char*)A + aoff[i] + (size_t)(kt) * 128), (PG8_LAS unsigned*)(MU_SA(buf) + wid * 1024 + i * 8192), 16, 0, 0); } while (0)
; #define MU_B_ISSUE(sb, kt) do { const char* kb_ = Bb + (size_t)(kt) * (64 * (size_t)RB); _Pragma("unroll") for (int j = 0; j < 8; ++j) { const char* p_ = kb_ + (size_t)j * RB; \
;         asm volatile("global_load_dwordx2 %0, %1, off" : "=&v"(sb[j]) : "v"(p_) : "memory"); } } while (0)
; #define MU_B_WAIT(sb, N) asm volatile("s_waitcnt vmcnt(%8)" : "+v"(sb[0]), "+v"(sb[1]), "+v"(sb[2]), "+v"(sb[3]), "+v"(sb[4]), "+v"(sb[5]), "+v"(sb[6]), "+v"(sb[7]) : "n"(N) : "memory")
; #define MU_COMPUTE(buf) MU_COMPUTE_N(buf, NMU)
; template <int MODE>
; __device__ __forceinline__ void moe_unit(PG8_LAS unsigned char* lds, int e, int cb, int slot0  , int nv  , const bf16_t* A, const int* slot_tok,
;                                          const float* W0, const float* W1, bf16_t* OUT, const float* slot_rs  , const int* slot_dst) {
;     ...
;     f32x4 acc[NMU][4];
; #pragma unroll
;     for (int m = 0; m < NMU; ++m)
; #pragma unroll
;         for (int n = 0; n < 4; ++n) acc[m][n] = (f32x4){0.f, 0.f, 0.f, 0.f};
;     f32x2 s0[8], s1[8];
;     float g0[8];
;     MU_GLDS_A(0, 0); MU_B_ISSUE(s0, 0); MU_G_LOAD(g0, 0); MU_B_ISSUE(s1, 1);
;     MU_B_WAIT(s0, 8); MU_B_WRITE(s0, 0, g0); __builtin_amdgcn_sched_barrier(0); MU_B_ISSUE(s0, 2);
;     asm volatile("s_waitcnt vmcnt(16)" ::: "memory");
;     asm volatile("s_waitcnt lgkmcnt(0)" ::: "memory"); __builtin_amdgcn_s_barrier(); asm volatile("" ::: "memory");
; #pragma unroll 1
;     for (int t = 0; t < nt; t += 2) {
;         if (t + 2 < nt) MU_B_WAIT(s1, 8); else MU_B_WAIT(s1, 0);
;         MU_G_LOAD(g0, t + 1); MU_B_WRITE(s1, 1, g0); __builtin_amdgcn_sched_barrier(0); MU_GLDS_A(1, t + 1); __builtin_amdgcn_sched_barrier(0);
;         if (t + 3 < nt) { MU_B_ISSUE(s1, t + 3); }
;         MU_COMPUTE(0);
;         MU_END(t + 3 >= nt);
;         if (t + 2 < nt) { MU_B_WAIT(s0, 8); MU_G_LOAD(g0, t + 2); MU_B_WRITE(s0, 0, g0); __builtin_amdgcn_sched_barrier(0); MU_GLDS_A(0, t + 2); __builtin_amdgcn_sched_barrier(0); }
;         if (t + 4 < nt) { MU_B_ISSUE(s0, t + 4); }
;         MU_COMPUTE(1);
;         MU_END(t + 4 >= nt);
	v_mul_f32_e32 v186, s12, v186
	v_mul_f32_e32 v187, s12, v187
	v_mul_f32_e32 v188, s13, v188
	v_mul_f32_e32 v189, s13, v189
	v_mul_f32_e32 v190, s14, v190
	v_mul_f32_e32 v191, s14, v191
	v_mul_f32_e32 v192, s15, v192
	v_mul_f32_e32 v193, s15, v193
	v_mul_f32_e32 v194, s16, v194
	v_mul_f32_e32 v195, s16, v195
	v_mul_f32_e32 v196, s17, v196
	v_mul_f32_e32 v197, s17, v197
	v_mul_f32_e32 v198, s18, v198
	v_mul_f32_e32 v199, s18, v199
	v_mul_f32_e32 v200, s19, v200
	v_mul_f32_e32 v201, s19, v201
	v_cvt_pk_bf16_f32 v158, v186, v188
	v_cvt_pk_bf16_f32 v159, v190, v192
	v_cvt_pk_bf16_f32 v160, v194, v196
	v_cvt_pk_bf16_f32 v161, v198, v200
	v_cvt_pk_bf16_f32 v162, v187, v189
	v_cvt_pk_bf16_f32 v163, v191, v193
	v_cvt_pk_bf16_f32 v164, v195, v197
	v_cvt_pk_bf16_f32 v165, v199, v201
	ds_write_b128 v1, v[158:161] offset:0
	ds_write_b128 v1, v[162:165] offset:128
	v_add_u32_e32 v91, s42, v135
	v_add_u32_e32 v93, s42, v137
	ds_read_b128 v[238:241], v139 offset:19456
	ds_read_b128 v[242:245], v139 offset:21504
	ds_read_b128 v[246:249], v139 offset:23552
	ds_read_b128 v[250:253], v139 offset:25600
	ds_read_b128 v[218:221], v91 offset:0
	ds_read_b128 v[222:225], v91 offset:2048
	ds_read_b128 v[226:229], v91 offset:4096
	ds_read_b128 v[230:233], v91 offset:6144
	s_waitcnt lgkmcnt(0)
	s_load_dwordx8 s[20:27], s[28:29], 0x0
	s_add_u32 s28, s28, 0x100
	s_addc_u32 s29, s29, 0
	v_mfma_f32_16x16x32_bf16 v[78:81], v[238:241], v[218:221], v[78:81]
	v_mfma_f32_16x16x32_bf16 v[74:77], v[242:245], v[218:221], v[74:77]
	v_mfma_f32_16x16x32_bf16 v[70:73], v[246:249], v[218:221], v[70:73]
	v_mfma_f32_16x16x32_bf16 v[66:69], v[250:253], v[218:221], v[66:69]
	ds_read_b128 v[218:221], v93 offset:0
	ds_read_b128 v[142:145], v141 offset:19456
	v_lshl_add_u64 v[132:133], v[132:133], 0, s[40:41]
	global_load_dwordx2 v[186:187], v[132:133], off
	global_load_dwordx2 v[188:189], v[132:133], off offset:2048
	v_mfma_f32_16x16x32_bf16 v[62:65], v[238:241], v[222:225], v[62:65]
	v_mfma_f32_16x16x32_bf16 v[58:61], v[242:245], v[222:225], v[58:61]
	v_mfma_f32_16x16x32_bf16 v[54:57], v[246:249], v[222:225], v[54:57]
	v_mfma_f32_16x16x32_bf16 v[50:53], v[250:253], v[222:225], v[50:53]
	ds_read_b128 v[222:225], v93 offset:2048
	ds_read_b128 v[146:149], v141 offset:21504
	v_lshl_add_u64 v[166:167], v[132:133], 0, s[34:35]
	global_load_dwordx2 v[190:191], v[166:167], off
	global_load_dwordx2 v[192:193], v[166:167], off offset:2048
	v_mfma_f32_16x16x32_bf16 v[46:49], v[238:241], v[226:229], v[46:49]
	v_mfma_f32_16x16x32_bf16 v[42:45], v[242:245], v[226:229], v[42:45]
	v_mfma_f32_16x16x32_bf16 v[38:41], v[246:249], v[226:229], v[38:41]
	v_mfma_f32_16x16x32_bf16 v[34:37], v[250:253], v[226:229], v[34:37]
	ds_read_b128 v[226:229], v93 offset:4096
	ds_read_b128 v[150:153], v141 offset:23552
	v_lshl_add_u64 v[166:167], v[132:133], 0, s[36:37]
	global_load_dwordx2 v[194:195], v[166:167], off
	global_load_dwordx2 v[196:197], v[166:167], off offset:2048
	v_mfma_f32_16x16x32_bf16 v[18:21], v[238:241], v[230:233], v[18:21]
	v_mfma_f32_16x16x32_bf16 v[22:25], v[242:245], v[230:233], v[22:25]
	v_mfma_f32_16x16x32_bf16 v[26:29], v[246:249], v[230:233], v[26:29]
	v_mfma_f32_16x16x32_bf16 v[30:33], v[250:253], v[230:233], v[30:33]
	ds_read_b128 v[230:233], v93 offset:6144
	ds_read_b128 v[154:157], v141 offset:25600
	v_lshl_add_u64 v[166:167], v[132:133], 0, s[38:39]
	global_load_dwordx2 v[198:199], v[166:167], off
	global_load_dwordx2 v[200:201], v[166:167], off offset:2048
	s_waitcnt vmcnt(21)
	s_waitcnt lgkmcnt(0)
	s_barrier
	s_mov_b32 s47, s42
	s_mov_b32 s42, s43
	s_mov_b32 s43, s44
	s_mov_b32 s44, s47
	s_add_i32 s47, s44, s6
	s_add_u32 s30, s30, 0x80
	s_addc_u32 s31, s31, 0
	v_mfma_f32_16x16x32_bf16 v[78:81], v[142:145], v[218:221], v[78:81]
	v_mfma_f32_16x16x32_bf16 v[74:77], v[146:149], v[218:221], v[74:77]
	v_mfma_f32_16x16x32_bf16 v[70:73], v[150:153], v[218:221], v[70:73]
	v_mfma_f32_16x16x32_bf16 v[66:69], v[154:157], v[218:221], v[66:69]
	s_mov_b32 m0, s47
	s_nop 0
	global_load_lds_dwordx4 v86, s[30:31]
	v_mfma_f32_16x16x32_bf16 v[62:65], v[142:145], v[222:225], v[62:65]
	v_mfma_f32_16x16x32_bf16 v[58:61], v[146:149], v[222:225], v[58:61]
	v_mfma_f32_16x16x32_bf16 v[54:57], v[150:153], v[222:225], v[54:57]
	v_mfma_f32_16x16x32_bf16 v[50:53], v[154:157], v[222:225], v[50:53]
	s_add_i32 m0, s47, 0x2000
	s_nop 0
	global_load_lds_dwordx4 v134, s[30:31]
	v_mfma_f32_16x16x32_bf16 v[46:49], v[142:145], v[226:229], v[46:49]
	v_mfma_f32_16x16x32_bf16 v[42:45], v[146:149], v[226:229], v[42:45]
	v_mfma_f32_16x16x32_bf16 v[38:41], v[150:153], v[226:229], v[38:41]
	v_mfma_f32_16x16x32_bf16 v[34:37], v[154:157], v[226:229], v[34:37]
	s_add_i32 m0, s47, 0x4000
	s_nop 0
	global_load_lds_dwordx4 v136, s[30:31]
	v_mfma_f32_16x16x32_bf16 v[18:21], v[142:145], v[230:233], v[18:21]
	v_mfma_f32_16x16x32_bf16 v[22:25], v[146:149], v[230:233], v[22:25]
	v_mfma_f32_16x16x32_bf16 v[26:29], v[150:153], v[230:233], v[26:29]
	v_mfma_f32_16x16x32_bf16 v[30:33], v[154:157], v[230:233], v[30:33]
	s_add_i32 m0, s47, 0x6000
	s_nop 0
	global_load_lds_dwordx4 v138, s[30:31]
	s_add_i32 m0, s47, 0x8000
	s_nop 0
	global_load_lds_dwordx4 v140, s[30:31]
	v_mul_f32_e32 v202, s20, v202
	v_mul_f32_e32 v203, s20, v203
	v_mul_f32_e32 v204, s21, v204
	v_mul_f32_e32 v205, s21, v205
	v_mul_f32_e32 v206, s22, v206
	v_mul_f32_e32 v207, s22, v207
	v_mul_f32_e32 v208, s23, v208
	v_mul_f32_e32 v209, s23, v209
	v_mul_f32_e32 v210, s24, v210
	v_mul_f32_e32 v211, s24, v211
	v_mul_f32_e32 v212, s25, v212
	v_mul_f32_e32 v213, s25, v213
	v_mul_f32_e32 v214, s26, v214
	v_mul_f32_e32 v215, s26, v215
	v_mul_f32_e32 v216, s27, v216
	v_mul_f32_e32 v217, s27, v217
	v_cvt_pk_bf16_f32 v158, v202, v204
	v_cvt_pk_bf16_f32 v159, v206, v208
	v_cvt_pk_bf16_f32 v160, v210, v212
	v_cvt_pk_bf16_f32 v161, v214, v216
	v_cvt_pk_bf16_f32 v162, v203, v205
	v_cvt_pk_bf16_f32 v163, v207, v209
	v_cvt_pk_bf16_f32 v164, v211, v213
	v_cvt_pk_bf16_f32 v165, v215, v217
	ds_write_b128 v1, v[158:161] offset:19456
	ds_write_b128 v1, v[162:165] offset:19584
	v_add_u32_e32 v91, s42, v135
	v_add_u32_e32 v93, s42, v137
	ds_read_b128 v[238:241], v139 offset:0
	ds_read_b128 v[242:245], v139 offset:2048
	ds_read_b128 v[246:249], v139 offset:4096
	ds_read_b128 v[250:253], v139 offset:6144
	ds_read_b128 v[218:221], v91 offset:0
	ds_read_b128 v[222:225], v91 offset:2048
	ds_read_b128 v[226:229], v91 offset:4096
	ds_read_b128 v[230:233], v91 offset:6144
	s_waitcnt lgkmcnt(0)
; #define MU_GLDS_A(buf, kt) do { _Pragma("unroll") for (int i = 0; i < NMU; ++i) \
;         __builtin_amdgcn_global_load_lds((const unsigned*)((const char*)A + aoff[i] + (size_t)(kt) * 128), (PG8_LAS unsigned*)(MU_SA(buf) + wid * 1024 + i * 8192), 16, 0, 0); } while (0)
; #define MU_B_ISSUE(sb, kt) do { const char* kb_ = Bb + (size_t)(kt) * (64 * (size_t)RB); _Pragma("unroll") for (int j = 0; j < 8; ++j) { const char* p_ = kb_ + (size_t)j * RB; \
;         asm volatile("global_load_dwordx2 %0, %1, off" : "=&v"(sb[j]) : "v"(p_) : "memory"); } } while (0)
; #define MU_B_WAIT(sb, N) asm volatile("s_waitcnt vmcnt(%8)" : "+v"(sb[0]), "+v"(sb[1]), "+v"(sb[2]), "+v"(sb[3]), "+v"(sb[4]), "+v"(sb[5]), "+v"(sb[6]), "+v"(sb[7]) : "n"(N) : "memory")
; #define MU_G_LOAD(ga, kt) do { const PG8_LAS f32x4* gk_ = (const PG8_LAS f32x4*)(lds + GAIN_OFF) + 16 * (kt) + 2 * wid; const f32x4 ga_ = gk_[0], gb_ = gk_[1]; \
;         ga[0] = ga_[0]; ga[1] = ga_[1]; ga[2] = ga_[2]; ga[3] = ga_[3]; ga[4] = gb_[0]; ga[5] = gb_[1]; ga[6] = gb_[2]; ga[7] = gb_[3]; } while (0)
; #define MU_COMPUTE(buf) MU_COMPUTE_N(buf, NMU)
; #define MU_END(last) do { if (last) asm volatile("s_waitcnt vmcnt(0)" ::: "memory"); else asm volatile("s_waitcnt vmcnt(8)" ::: "memory"); \
;         asm volatile("s_waitcnt lgkmcnt(0)" ::: "memory"); __builtin_amdgcn_s_barrier(); asm volatile("" ::: "memory"); } while (0)
; template <int MODE>
; __device__ __forceinline__ void moe_unit(PG8_LAS unsigned char* lds, int e, int cb, int slot0  , int nv  , const bf16_t* A, const int* slot_tok,
;                                          const float* W0, const float* W1, bf16_t* OUT, const float* slot_rs  , const int* slot_dst) {
;     ...
;     for (int t = 0; t < nt; t += 2) {
;         if (t + 2 < nt) MU_B_WAIT(s1, 8); else MU_B_WAIT(s1, 0);
;         MU_G_LOAD(g0, t + 1); MU_B_WRITE(s1, 1, g0); __builtin_amdgcn_sched_barrier(0); MU_GLDS_A(1, t + 1); __builtin_amdgcn_sched_barrier(0);
;         if (t + 3 < nt) { MU_B_ISSUE(s1, t + 3); }
;         MU_COMPUTE(0);
;         MU_END(t + 3 >= nt);
	s_load_dwordx8 s[12:19], s[28:29], 0x0
	s_add_u32 s28, s28, 0x100
	s_addc_u32 s29, s29, 0
	v_mfma_f32_16x16x32_bf16 v[78:81], v[238:241], v[218:221], v[78:81]
	v_mfma_f32_16x16x32_bf16 v[74:77], v[242:245], v[218:221], v[74:77]
	v_mfma_f32_16x16x32_bf16 v[70:73], v[246:249], v[218:221], v[70:73]
	v_mfma_f32_16x16x32_bf16 v[66:69], v[250:253], v[218:221], v[66:69]
	ds_read_b128 v[218:221], v93 offset:0
	ds_read_b128 v[142:145], v141 offset:0
	v_lshl_add_u64 v[132:133], v[132:133], 0, s[40:41]
	global_load_dwordx2 v[202:203], v[132:133], off
	global_load_dwordx2 v[204:205], v[132:133], off offset:2048
	v_mfma_f32_16x16x32_bf16 v[62:65], v[238:241], v[222:225], v[62:65]
	v_mfma_f32_16x16x32_bf16 v[58:61], v[242:245], v[222:225], v[58:61]
	v_mfma_f32_16x16x32_bf16 v[54:57], v[246:249], v[222:225], v[54:57]
	v_mfma_f32_16x16x32_bf16 v[50:53], v[250:253], v[222:225], v[50:53]
	ds_read_b128 v[222:225], v93 offset:2048
	ds_read_b128 v[146:149], v141 offset:2048
	v_lshl_add_u64 v[166:167], v[132:133], 0, s[34:35]
	global_load_dwordx2 v[206:207], v[166:167], off
	global_load_dwordx2 v[208:209], v[166:167], off offset:2048
	v_mfma_f32_16x16x32_bf16 v[46:49], v[238:241], v[226:229], v[46:49]
	v_mfma_f32_16x16x32_bf16 v[42:45], v[242:245], v[226:229], v[42:45]
	v_mfma_f32_16x16x32_bf16 v[38:41], v[246:249], v[226:229], v[38:41]
	v_mfma_f32_16x16x32_bf16 v[34:37], v[250:253], v[226:229], v[34:37]
	ds_read_b128 v[226:229], v93 offset:4096
	ds_read_b128 v[150:153], v141 offset:4096
	v_lshl_add_u64 v[166:167], v[132:133], 0, s[36:37]
	global_load_dwordx2 v[210:211], v[166:167], off
	global_load_dwordx2 v[212:213], v[166:167], off offset:2048
	v_mfma_f32_16x16x32_bf16 v[18:21], v[238:241], v[230:233], v[18:21]
	v_mfma_f32_16x16x32_bf16 v[22:25], v[242:245], v[230:233], v[22:25]
	v_mfma_f32_16x16x32_bf16 v[26:29], v[246:249], v[230:233], v[26:29]
	v_mfma_f32_16x16x32_bf16 v[30:33], v[250:253], v[230:233], v[30:33]
	ds_read_b128 v[230:233], v93 offset:6144
	ds_read_b128 v[154:157], v141 offset:6144
	v_lshl_add_u64 v[166:167], v[132:133], 0, s[38:39]
	global_load_dwordx2 v[214:215], v[166:167], off
	global_load_dwordx2 v[216:217], v[166:167], off offset:2048
	s_waitcnt vmcnt(21)
	s_waitcnt lgkmcnt(0)
	s_barrier
; #define MU_GLDS_A(buf, kt) do { _Pragma("unroll") for (int i = 0; i < NMU; ++i) \
;         __builtin_amdgcn_global_load_lds((const unsigned*)((const char*)A + aoff[i] + (size_t)(kt) * 128), (PG8_LAS unsigned*)(MU_SA(buf) + wid * 1024 + i * 8192), 16, 0, 0); } while (0)
; #define MU_B_ISSUE(sb, kt) do { const char* kb_ = Bb + (size_t)(kt) * (64 * (size_t)RB); _Pragma("unroll") for (int j = 0; j < 8; ++j) { const char* p_ = kb_ + (size_t)j * RB; \
;         asm volatile("global_load_dwordx2 %0, %1, off" : "=&v"(sb[j]) : "v"(p_) : "memory"); } } while (0)
; #define MU_B_WAIT(sb, N) asm volatile("s_waitcnt vmcnt(%8)" : "+v"(sb[0]), "+v"(sb[1]), "+v"(sb[2]), "+v"(sb[3]), "+v"(sb[4]), "+v"(sb[5]), "+v"(sb[6]), "+v"(sb[7]) : "n"(N) : "memory")
; #define MU_COMPUTE(buf) MU_COMPUTE_N(buf, NMU)
; template <int MODE>
; __device__ __forceinline__ void moe_unit(PG8_LAS unsigned char* lds, int e, int cb, int slot0  , int nv  , const bf16_t* A, const int* slot_tok,
;                                          const float* W0, const float* W1, bf16_t* OUT, const float* slot_rs  , const int* slot_dst) {
;     ...
;     f32x4 acc[NMU][4];
; #pragma unroll
;     for (int m = 0; m < NMU; ++m)
; #pragma unroll
;         for (int n = 0; n < 4; ++n) acc[m][n] = (f32x4){0.f, 0.f, 0.f, 0.f};
;     f32x2 s0[8], s1[8];
;     float g0[8];
;     MU_GLDS_A(0, 0); MU_B_ISSUE(s0, 0); MU_G_LOAD(g0, 0); MU_B_ISSUE(s1, 1);
;     MU_B_WAIT(s0, 8); MU_B_WRITE(s0, 0, g0); __builtin_amdgcn_sched_barrier(0); MU_B_ISSUE(s0, 2);
;     asm volatile("s_waitcnt vmcnt(16)" ::: "memory");
;     asm volatile("s_waitcnt lgkmcnt(0)" ::: "memory"); __builtin_amdgcn_s_barrier(); asm volatile("" ::: "memory");
; #pragma unroll 1
;     for (int t = 0; t < nt; t += 2) {
;         if (t + 2 < nt) MU_B_WAIT(s1, 8); else MU_B_WAIT(s1, 0);
;         MU_G_LOAD(g0, t + 1); MU_B_WRITE(s1, 1, g0); __builtin_amdgcn_sched_barrier(0); MU_GLDS_A(1, t + 1); __builtin_amdgcn_sched_barrier(0);
;         if (t + 3 < nt) { MU_B_ISSUE(s1, t + 3); }
;         MU_COMPUTE(0);
;         MU_END(t + 3 >= nt);
;         if (t + 2 < nt) { MU_B_WAIT(s0, 8); MU_G_LOAD(g0, t + 2); MU_B_WRITE(s0, 0, g0); __builtin_amdgcn_sched_barrier(0); MU_GLDS_A(0, t + 2); __builtin_amdgcn_sched_barrier(0); }
;         if (t + 4 < nt) { MU_B_ISSUE(s0, t + 4); }
;         MU_COMPUTE(1);
;         MU_END(t + 4 >= nt);
	s_mov_b32 s47, s42
	s_mov_b32 s42, s43
	s_mov_b32 s43, s44
	s_mov_b32 s44, s47
	s_add_i32 s47, s44, s6
	s_add_u32 s30, s30, 0x80
	s_addc_u32 s31, s31, 0
	v_mfma_f32_16x16x32_bf16 v[78:81], v[142:145], v[218:221], v[78:81]
	v_mfma_f32_16x16x32_bf16 v[74:77], v[146:149], v[218:221], v[74:77]
	v_mfma_f32_16x16x32_bf16 v[70:73], v[150:153], v[218:221], v[70:73]
	v_mfma_f32_16x16x32_bf16 v[66:69], v[154:157], v[218:221], v[66:69]
	s_mov_b32 m0, s47
	s_nop 0
	global_load_lds_dwordx4 v86, s[30:31]
	v_mfma_f32_16x16x32_bf16 v[62:65], v[142:145], v[222:225], v[62:65]
	v_mfma_f32_16x16x32_bf16 v[58:61], v[146:149], v[222:225], v[58:61]
	v_mfma_f32_16x16x32_bf16 v[54:57], v[150:153], v[222:225], v[54:57]
	v_mfma_f32_16x16x32_bf16 v[50:53], v[154:157], v[222:225], v[50:53]
	s_add_i32 m0, s47, 0x2000
	s_nop 0
	global_load_lds_dwordx4 v134, s[30:31]
	v_mfma_f32_16x16x32_bf16 v[46:49], v[142:145], v[226:229], v[46:49]
	v_mfma_f32_16x16x32_bf16 v[42:45], v[146:149], v[226:229], v[42:45]
	v_mfma_f32_16x16x32_bf16 v[38:41], v[150:153], v[226:229], v[38:41]
	v_mfma_f32_16x16x32_bf16 v[34:37], v[154:157], v[226:229], v[34:37]
	s_add_i32 m0, s47, 0x4000
	s_nop 0
	global_load_lds_dwordx4 v136, s[30:31]
	v_mfma_f32_16x16x32_bf16 v[18:21], v[142:145], v[230:233], v[18:21]
	v_mfma_f32_16x16x32_bf16 v[22:25], v[146:149], v[230:233], v[22:25]
	v_mfma_f32_16x16x32_bf16 v[26:29], v[150:153], v[230:233], v[26:29]
	v_mfma_f32_16x16x32_bf16 v[30:33], v[154:157], v[230:233], v[30:33]
	s_add_i32 m0, s47, 0x6000
	s_nop 0
	global_load_lds_dwordx4 v138, s[30:31]
	s_add_i32 m0, s47, 0x8000
	s_nop 0
	global_load_lds_dwordx4 v140, s[30:31]
	v_mul_f32_e32 v98, s12, v98
	v_mul_f32_e32 v99, s12, v99
	v_mul_f32_e32 v100, s13, v100
	v_mul_f32_e32 v101, s13, v101
	v_mul_f32_e32 v102, s14, v102
	v_mul_f32_e32 v103, s14, v103
	v_mul_f32_e32 v104, s15, v104
	v_mul_f32_e32 v105, s15, v105
	v_mul_f32_e32 v106, s16, v106
	v_mul_f32_e32 v107, s16, v107
	v_mul_f32_e32 v108, s17, v108
	v_mul_f32_e32 v109, s17, v109
	v_mul_f32_e32 v110, s18, v110
	v_mul_f32_e32 v111, s18, v111
	v_mul_f32_e32 v112, s19, v112
	v_mul_f32_e32 v113, s19, v113
	v_cvt_pk_bf16_f32 v158, v98, v100
	v_cvt_pk_bf16_f32 v159, v102, v104
	v_cvt_pk_bf16_f32 v160, v106, v108
	v_cvt_pk_bf16_f32 v161, v110, v112
	v_cvt_pk_bf16_f32 v162, v99, v101
	v_cvt_pk_bf16_f32 v163, v103, v105
	v_cvt_pk_bf16_f32 v164, v107, v109
	v_cvt_pk_bf16_f32 v165, v111, v113
	ds_write_b128 v1, v[158:161] offset:0
	ds_write_b128 v1, v[162:165] offset:128
	v_add_u32_e32 v91, s42, v135
	v_add_u32_e32 v93, s42, v137
	ds_read_b128 v[238:241], v139 offset:19456
	ds_read_b128 v[242:245], v139 offset:21504
	ds_read_b128 v[246:249], v139 offset:23552
	ds_read_b128 v[250:253], v139 offset:25600
	ds_read_b128 v[218:221], v91 offset:0
	ds_read_b128 v[222:225], v91 offset:2048
	ds_read_b128 v[226:229], v91 offset:4096
	ds_read_b128 v[230:233], v91 offset:6144
	s_waitcnt lgkmcnt(0)
	s_load_dwordx8 s[20:27], s[28:29], 0x0
	s_add_u32 s28, s28, 0x100
	s_addc_u32 s29, s29, 0
	v_mfma_f32_16x16x32_bf16 v[78:81], v[238:241], v[218:221], v[78:81]
	v_mfma_f32_16x16x32_bf16 v[74:77], v[242:245], v[218:221], v[74:77]
	v_mfma_f32_16x16x32_bf16 v[70:73], v[246:249], v[218:221], v[70:73]
	v_mfma_f32_16x16x32_bf16 v[66:69], v[250:253], v[218:221], v[66:69]
	ds_read_b128 v[218:221], v93 offset:0
	ds_read_b128 v[142:145], v141 offset:19456
	v_lshl_add_u64 v[132:133], v[132:133], 0, s[40:41]
	global_load_dwordx2 v[98:99], v[132:133], off
	global_load_dwordx2 v[100:101], v[132:133], off offset:2048
	v_mfma_f32_16x16x32_bf16 v[62:65], v[238:241], v[222:225], v[62:65]
	v_mfma_f32_16x16x32_bf16 v[58:61], v[242:245], v[222:225], v[58:61]
	v_mfma_f32_16x16x32_bf16 v[54:57], v[246:249], v[222:225], v[54:57]
	v_mfma_f32_16x16x32_bf16 v[50:53], v[250:253], v[222:225], v[50:53]
	ds_read_b128 v[222:225], v93 offset:2048
	ds_read_b128 v[146:149], v141 offset:21504
	v_lshl_add_u64 v[166:167], v[132:133], 0, s[34:35]
	global_load_dwordx2 v[102:103], v[166:167], off
	global_load_dwordx2 v[104:105], v[166:167], off offset:2048
	v_mfma_f32_16x16x32_bf16 v[46:49], v[238:241], v[226:229], v[46:49]
	v_mfma_f32_16x16x32_bf16 v[42:45], v[242:245], v[226:229], v[42:45]
	v_mfma_f32_16x16x32_bf16 v[38:41], v[246:249], v[226:229], v[38:41]
	v_mfma_f32_16x16x32_bf16 v[34:37], v[250:253], v[226:229], v[34:37]
	ds_read_b128 v[226:229], v93 offset:4096
	ds_read_b128 v[150:153], v141 offset:23552
	v_lshl_add_u64 v[166:167], v[132:133], 0, s[36:37]
	global_load_dwordx2 v[106:107], v[166:167], off
	global_load_dwordx2 v[108:109], v[166:167], off offset:2048
	v_mfma_f32_16x16x32_bf16 v[18:21], v[238:241], v[230:233], v[18:21]
	v_mfma_f32_16x16x32_bf16 v[22:25], v[242:245], v[230:233], v[22:25]
	v_mfma_f32_16x16x32_bf16 v[26:29], v[246:249], v[230:233], v[26:29]
	v_mfma_f32_16x16x32_bf16 v[30:33], v[250:253], v[230:233], v[30:33]
	ds_read_b128 v[230:233], v93 offset:6144
	ds_read_b128 v[154:157], v141 offset:25600
	v_lshl_add_u64 v[166:167], v[132:133], 0, s[38:39]
	global_load_dwordx2 v[110:111], v[166:167], off
	global_load_dwordx2 v[112:113], v[166:167], off offset:2048
	s_waitcnt vmcnt(21)
	s_waitcnt lgkmcnt(0)
	s_barrier
	s_mov_b32 s47, s42
	s_mov_b32 s42, s43
	s_mov_b32 s43, s44
	s_mov_b32 s44, s47
	s_mov_b32 s46, 13

; #define MU_GLDS_A(buf, kt) do { _Pragma("unroll") for (int i = 0; i < NMU; ++i) \
;         __builtin_amdgcn_global_load_lds((const unsigned*)((const char*)A + aoff[i] + (size_t)(kt) * 128), (PG8_LAS unsigned*)(MU_SA(buf) + wid * 1024 + i * 8192), 16, 0, 0); } while (0)
; #define MU_B_ISSUE(sb, kt) do { const char* kb_ = Bb + (size_t)(kt) * (64 * (size_t)RB); _Pragma("unroll") for (int j = 0; j < 8; ++j) { const char* p_ = kb_ + (size_t)j * RB; \
;         asm volatile("global_load_dwordx2 %0, %1, off" : "=&v"(sb[j]) : "v"(p_) : "memory"); } } while (0)
; #define MU_B_WAIT(sb, N) asm volatile("s_waitcnt vmcnt(%8)" : "+v"(sb[0]), "+v"(sb[1]), "+v"(sb[2]), "+v"(sb[3]), "+v"(sb[4]), "+v"(sb[5]), "+v"(sb[6]), "+v"(sb[7]) : "n"(N) : "memory")
; #define MU_COMPUTE(buf) MU_COMPUTE_N(buf, NMU)
; template <int MODE>
; __device__ __forceinline__ void moe_unit(PG8_LAS unsigned char* lds, int e, int cb, int slot0  , int nv  , const bf16_t* A, const int* slot_tok,
;                                          const float* W0, const float* W1, bf16_t* OUT, const float* slot_rs  , const int* slot_dst) {
;     ...
;     f32x4 acc[NMU][4];
; #pragma unroll
;     for (int m = 0; m < NMU; ++m)
; #pragma unroll
;         for (int n = 0; n < 4; ++n) acc[m][n] = (f32x4){0.f, 0.f, 0.f, 0.f};
;     f32x2 s0[8], s1[8];
;     float g0[8];
;     MU_GLDS_A(0, 0); MU_B_ISSUE(s0, 0); MU_G_LOAD(g0, 0); MU_B_ISSUE(s1, 1);
;     MU_B_WAIT(s0, 8); MU_B_WRITE(s0, 0, g0); __builtin_amdgcn_sched_barrier(0); MU_B_ISSUE(s0, 2);
;     asm volatile("s_waitcnt vmcnt(16)" ::: "memory");
;     asm volatile("s_waitcnt lgkmcnt(0)" ::: "memory"); __builtin_amdgcn_s_barrier(); asm volatile("" ::: "memory");
; #pragma unroll 1
;     for (int t = 0; t < nt; t += 2) {
;         if (t + 2 < nt) MU_B_WAIT(s1, 8); else MU_B_WAIT(s1, 0);
;         MU_G_LOAD(g0, t + 1); MU_B_WRITE(s1, 1, g0); __builtin_amdgcn_sched_barrier(0); MU_GLDS_A(1, t + 1); __builtin_amdgcn_sched_barrier(0);
;         if (t + 3 < nt) { MU_B_ISSUE(s1, t + 3); }
;         MU_COMPUTE(0);
;         MU_END(t + 3 >= nt);
;         if (t + 2 < nt) { MU_B_WAIT(s0, 8); MU_G_LOAD(g0, t + 2); MU_B_WRITE(s0, 0, g0); __builtin_amdgcn_sched_barrier(0); MU_GLDS_A(0, t + 2); __builtin_amdgcn_sched_barrier(0); }
;         if (t + 4 < nt) { MU_B_ISSUE(s0, t + 4); }
;         MU_COMPUTE(1);
;         MU_END(t + 4 >= nt);
.Lmu_grpY5:
	s_setprio 1
	s_add_i32 s47, s44, s6
	s_add_u32 s30, s30, 0x80
	s_addc_u32 s31, s31, 0
	s_mov_b32 m0, s47
	s_nop 0
	global_load_lds_dwordx4 v86, s[30:31]
	s_add_i32 m0, s47, 0x2000
	s_nop 0
	global_load_lds_dwordx4 v134, s[30:31]
	s_add_i32 m0, s47, 0x4000
	s_nop 0
	global_load_lds_dwordx4 v136, s[30:31]
	s_add_i32 m0, s47, 0x6000
	s_nop 0
	global_load_lds_dwordx4 v138, s[30:31]
	s_add_i32 m0, s47, 0x8000
	s_nop 0
	global_load_lds_dwordx4 v140, s[30:31]
	s_waitcnt vmcnt(29)
	v_mul_f32_e32 v114, s20, v114
	v_mul_f32_e32 v115, s20, v115
	v_mul_f32_e32 v116, s21, v116
	v_mul_f32_e32 v117, s21, v117
	v_mul_f32_e32 v118, s22, v118
	v_mul_f32_e32 v119, s22, v119
	v_mul_f32_e32 v120, s23, v120
	v_mul_f32_e32 v121, s23, v121
	v_mul_f32_e32 v122, s24, v122
	v_mul_f32_e32 v123, s24, v123
	v_mul_f32_e32 v124, s25, v124
	v_mul_f32_e32 v125, s25, v125
	v_mul_f32_e32 v126, s26, v126
	v_mul_f32_e32 v127, s26, v127
	v_mul_f32_e32 v128, s27, v128
	v_mul_f32_e32 v129, s27, v129
	v_cvt_pk_bf16_f32 v158, v114, v116
	v_cvt_pk_bf16_f32 v159, v118, v120
	v_cvt_pk_bf16_f32 v160, v122, v124
	v_cvt_pk_bf16_f32 v161, v126, v128
	v_cvt_pk_bf16_f32 v162, v115, v117
	v_cvt_pk_bf16_f32 v163, v119, v121
	v_cvt_pk_bf16_f32 v164, v123, v125
	v_cvt_pk_bf16_f32 v165, v127, v129
	ds_write_b128 v1, v[158:161] offset:19456
	ds_write_b128 v1, v[162:165] offset:19584
	v_add_u32_e32 v91, s42, v135
	v_add_u32_e32 v93, s42, v137
	ds_read_b128 v[238:241], v139 offset:0
	ds_read_b128 v[242:245], v139 offset:2048
	ds_read_b128 v[246:249], v139 offset:4096
	ds_read_b128 v[250:253], v139 offset:6144
	ds_read_b128 v[218:221], v91 offset:0
	ds_read_b128 v[222:225], v91 offset:2048
	ds_read_b128 v[226:229], v91 offset:4096
	ds_read_b128 v[230:233], v91 offset:6144
	ds_read_b128 v[234:237], v91 offset:8192
	s_waitcnt lgkmcnt(0)
	s_load_dwordx8 s[12:19], s[28:29], 0x0
	s_add_u32 s28, s28, 0x100
	s_addc_u32 s29, s29, 0
	v_mfma_f32_16x16x32_bf16 v[78:81], v[238:241], v[218:221], v[78:81]
	v_mfma_f32_16x16x32_bf16 v[74:77], v[242:245], v[218:221], v[74:77]
	v_mfma_f32_16x16x32_bf16 v[70:73], v[246:249], v[218:221], v[70:73]
	v_mfma_f32_16x16x32_bf16 v[66:69], v[250:253], v[218:221], v[66:69]
	ds_read_b128 v[218:221], v93 offset:0
	ds_read_b128 v[142:145], v141 offset:0
	v_lshl_add_u64 v[132:133], v[132:133], 0, s[40:41]
	global_load_dwordx2 v[114:115], v[132:133], off
	global_load_dwordx2 v[116:117], v[132:133], off offset:2048
	v_mfma_f32_16x16x32_bf16 v[62:65], v[238:241], v[222:225], v[62:65]
	v_mfma_f32_16x16x32_bf16 v[58:61], v[242:245], v[222:225], v[58:61]
	v_mfma_f32_16x16x32_bf16 v[54:57], v[246:249], v[222:225], v[54:57]
	v_mfma_f32_16x16x32_bf16 v[50:53], v[250:253], v[222:225], v[50:53]
	ds_read_b128 v[222:225], v93 offset:2048
	ds_read_b128 v[146:149], v141 offset:2048
	v_lshl_add_u64 v[166:167], v[132:133], 0, s[34:35]
	global_load_dwordx2 v[118:119], v[166:167], off
	global_load_dwordx2 v[120:121], v[166:167], off offset:2048
	v_mfma_f32_16x16x32_bf16 v[46:49], v[238:241], v[226:229], v[46:49]
	v_mfma_f32_16x16x32_bf16 v[42:45], v[242:245], v[226:229], v[42:45]
	v_mfma_f32_16x16x32_bf16 v[38:41], v[246:249], v[226:229], v[38:41]
	v_mfma_f32_16x16x32_bf16 v[34:37], v[250:253], v[226:229], v[34:37]
	ds_read_b128 v[226:229], v93 offset:4096
	ds_read_b128 v[150:153], v141 offset:4096
	v_lshl_add_u64 v[166:167], v[132:133], 0, s[36:37]
	global_load_dwordx2 v[122:123], v[166:167], off
	global_load_dwordx2 v[124:125], v[166:167], off offset:2048
	v_mfma_f32_16x16x32_bf16 v[18:21], v[238:241], v[230:233], v[18:21]
	v_mfma_f32_16x16x32_bf16 v[22:25], v[242:245], v[230:233], v[22:25]
	v_mfma_f32_16x16x32_bf16 v[26:29], v[246:249], v[230:233], v[26:29]
	v_mfma_f32_16x16x32_bf16 v[30:33], v[250:253], v[230:233], v[30:33]
	ds_read_b128 v[230:233], v93 offset:6144
	ds_read_b128 v[154:157], v141 offset:6144
	v_lshl_add_u64 v[166:167], v[132:133], 0, s[38:39]
	global_load_dwordx2 v[126:127], v[166:167], off
	global_load_dwordx2 v[128:129], v[166:167], off offset:2048
	v_mfma_f32_16x16x32_bf16 v[2:5], v[238:241], v[234:237], v[2:5]
	v_mfma_f32_16x16x32_bf16 v[6:9], v[242:245], v[234:237], v[6:9]
	v_mfma_f32_16x16x32_bf16 v[10:13], v[246:249], v[234:237], v[10:13]
	v_mfma_f32_16x16x32_bf16 v[14:17], v[250:253], v[234:237], v[14:17]
	ds_read_b128 v[234:237], v93 offset:8192
	s_waitcnt lgkmcnt(0)
	s_barrier
; #define MU_GLDS_A(buf, kt) do { _Pragma("unroll") for (int i = 0; i < NMU; ++i) \
;         __builtin_amdgcn_global_load_lds((const unsigned*)((const char*)A + aoff[i] + (size_t)(kt) * 128), (PG8_LAS unsigned*)(MU_SA(buf) + wid * 1024 + i * 8192), 16, 0, 0); } while (0)
; #define MU_B_ISSUE(sb, kt) do { const char* kb_ = Bb + (size_t)(kt) * (64 * (size_t)RB); _Pragma("unroll") for (int j = 0; j < 8; ++j) { const char* p_ = kb_ + (size_t)j * RB; \
;         asm volatile("global_load_dwordx2 %0, %1, off" : "=&v"(sb[j]) : "v"(p_) : "memory"); } } while (0)
; #define MU_B_WAIT(sb, N) asm volatile("s_waitcnt vmcnt(%8)" : "+v"(sb[0]), "+v"(sb[1]), "+v"(sb[2]), "+v"(sb[3]), "+v"(sb[4]), "+v"(sb[5]), "+v"(sb[6]), "+v"(sb[7]) : "n"(N) : "memory")
; #define MU_COMPUTE(buf) MU_COMPUTE_N(buf, NMU)
; template <int MODE>
; __device__ __forceinline__ void moe_unit(PG8_LAS unsigned char* lds, int e, int cb, int slot0  , int nv  , const bf16_t* A, const int* slot_tok,
;                                          const float* W0, const float* W1, bf16_t* OUT, const float* slot_rs  , const int* slot_dst) {
;     ...
;     f32x4 acc[NMU][4];
; #pragma unroll
;     for (int m = 0; m < NMU; ++m)
; #pragma unroll
;         for (int n = 0; n < 4; ++n) acc[m][n] = (f32x4){0.f, 0.f, 0.f, 0.f};
;     f32x2 s0[8], s1[8];
;     float g0[8];
;     MU_GLDS_A(0, 0); MU_B_ISSUE(s0, 0); MU_G_LOAD(g0, 0); MU_B_ISSUE(s1, 1);
;     MU_B_WAIT(s0, 8); MU_B_WRITE(s0, 0, g0); __builtin_amdgcn_sched_barrier(0); MU_B_ISSUE(s0, 2);
;     asm volatile("s_waitcnt vmcnt(16)" ::: "memory");
;     asm volatile("s_waitcnt lgkmcnt(0)" ::: "memory"); __builtin_amdgcn_s_barrier(); asm volatile("" ::: "memory");
; #pragma unroll 1
;     for (int t = 0; t < nt; t += 2) {
;         if (t + 2 < nt) MU_B_WAIT(s1, 8); else MU_B_WAIT(s1, 0);
;         MU_G_LOAD(g0, t + 1); MU_B_WRITE(s1, 1, g0); __builtin_amdgcn_sched_barrier(0); MU_GLDS_A(1, t + 1); __builtin_amdgcn_sched_barrier(0);
;         if (t + 3 < nt) { MU_B_ISSUE(s1, t + 3); }
;         MU_COMPUTE(0);
;         MU_END(t + 3 >= nt);
;         if (t + 2 < nt) { MU_B_WAIT(s0, 8); MU_G_LOAD(g0, t + 2); MU_B_WRITE(s0, 0, g0); __builtin_amdgcn_sched_barrier(0); MU_GLDS_A(0, t + 2); __builtin_amdgcn_sched_barrier(0); }
;         if (t + 4 < nt) { MU_B_ISSUE(s0, t + 4); }
;         MU_COMPUTE(1);
;         MU_END(t + 4 >= nt);
	s_mov_b32 s47, s42
	s_mov_b32 s42, s43
	s_mov_b32 s43, s44
	s_mov_b32 s44, s47
	s_add_i32 s47, s44, s6
	s_add_u32 s30, s30, 0x80
	s_addc_u32 s31, s31, 0
	v_mfma_f32_16x16x32_bf16 v[78:81], v[142:145], v[218:221], v[78:81]
	v_mfma_f32_16x16x32_bf16 v[74:77], v[146:149], v[218:221], v[74:77]
	v_mfma_f32_16x16x32_bf16 v[70:73], v[150:153], v[218:221], v[70:73]
	v_mfma_f32_16x16x32_bf16 v[66:69], v[154:157], v[218:221], v[66:69]
	s_mov_b32 m0, s47
	s_nop 0
	global_load_lds_dwordx4 v86, s[30:31]
	v_mfma_f32_16x16x32_bf16 v[62:65], v[142:145], v[222:225], v[62:65]
	v_mfma_f32_16x16x32_bf16 v[58:61], v[146:149], v[222:225], v[58:61]
	v_mfma_f32_16x16x32_bf16 v[54:57], v[150:153], v[222:225], v[54:57]
	v_mfma_f32_16x16x32_bf16 v[50:53], v[154:157], v[222:225], v[50:53]
	s_add_i32 m0, s47, 0x2000
	s_nop 0
	global_load_lds_dwordx4 v134, s[30:31]
	v_mfma_f32_16x16x32_bf16 v[46:49], v[142:145], v[226:229], v[46:49]
	v_mfma_f32_16x16x32_bf16 v[42:45], v[146:149], v[226:229], v[42:45]
	v_mfma_f32_16x16x32_bf16 v[38:41], v[150:153], v[226:229], v[38:41]
	v_mfma_f32_16x16x32_bf16 v[34:37], v[154:157], v[226:229], v[34:37]
	s_add_i32 m0, s47, 0x4000
	s_nop 0
	global_load_lds_dwordx4 v136, s[30:31]
	v_mfma_f32_16x16x32_bf16 v[18:21], v[142:145], v[230:233], v[18:21]
	v_mfma_f32_16x16x32_bf16 v[22:25], v[146:149], v[230:233], v[22:25]
	v_mfma_f32_16x16x32_bf16 v[26:29], v[150:153], v[230:233], v[26:29]
	v_mfma_f32_16x16x32_bf16 v[30:33], v[154:157], v[230:233], v[30:33]
	s_add_i32 m0, s47, 0x6000
	s_nop 0
	global_load_lds_dwordx4 v138, s[30:31]
	v_mfma_f32_16x16x32_bf16 v[2:5], v[142:145], v[234:237], v[2:5]
	v_mfma_f32_16x16x32_bf16 v[6:9], v[146:149], v[234:237], v[6:9]
	v_mfma_f32_16x16x32_bf16 v[10:13], v[150:153], v[234:237], v[10:13]
	v_mfma_f32_16x16x32_bf16 v[14:17], v[154:157], v[234:237], v[14:17]
	s_add_i32 m0, s47, 0x8000
	s_nop 0
	global_load_lds_dwordx4 v140, s[30:31]
	s_waitcnt vmcnt(34)
	v_mul_f32_e32 v186, s12, v186
	v_mul_f32_e32 v187, s12, v187
	v_mul_f32_e32 v188, s13, v188
	v_mul_f32_e32 v189, s13, v189
	v_mul_f32_e32 v190, s14, v190
	v_mul_f32_e32 v191, s14, v191
	v_mul_f32_e32 v192, s15, v192
	v_mul_f32_e32 v193, s15, v193
	v_mul_f32_e32 v194, s16, v194
	v_mul_f32_e32 v195, s16, v195
	v_mul_f32_e32 v196, s17, v196
	v_mul_f32_e32 v197, s17, v197
	v_mul_f32_e32 v198, s18, v198
	v_mul_f32_e32 v199, s18, v199
	v_mul_f32_e32 v200, s19, v200
	v_mul_f32_e32 v201, s19, v201
	v_cvt_pk_bf16_f32 v158, v186, v188
	v_cvt_pk_bf16_f32 v159, v190, v192
	v_cvt_pk_bf16_f32 v160, v194, v196
	v_cvt_pk_bf16_f32 v161, v198, v200
	v_cvt_pk_bf16_f32 v162, v187, v189
	v_cvt_pk_bf16_f32 v163, v191, v193
	v_cvt_pk_bf16_f32 v164, v195, v197
	v_cvt_pk_bf16_f32 v165, v199, v201
	ds_write_b128 v1, v[158:161] offset:0
	ds_write_b128 v1, v[162:165] offset:128
	v_add_u32_e32 v91, s42, v135
	v_add_u32_e32 v93, s42, v137
	ds_read_b128 v[238:241], v139 offset:19456
	ds_read_b128 v[242:245], v139 offset:21504
	ds_read_b128 v[246:249], v139 offset:23552
	ds_read_b128 v[250:253], v139 offset:25600
	ds_read_b128 v[218:221], v91 offset:0
	ds_read_b128 v[222:225], v91 offset:2048
	ds_read_b128 v[226:229], v91 offset:4096
	ds_read_b128 v[230:233], v91 offset:6144
	ds_read_b128 v[234:237], v91 offset:8192
	s_waitcnt lgkmcnt(0)
	s_load_dwordx8 s[20:27], s[28:29], 0x0
	s_add_u32 s28, s28, 0x100
	s_addc_u32 s29, s29, 0
	v_mfma_f32_16x16x32_bf16 v[78:81], v[238:241], v[218:221], v[78:81]
	v_mfma_f32_16x16x32_bf16 v[74:77], v[242:245], v[218:221], v[74:77]
	v_mfma_f32_16x16x32_bf16 v[70:73], v[246:249], v[218:221], v[70:73]
	v_mfma_f32_16x16x32_bf16 v[66:69], v[250:253], v[218:221], v[66:69]
	ds_read_b128 v[218:221], v93 offset:0
	ds_read_b128 v[142:145], v141 offset:19456
	v_lshl_add_u64 v[132:133], v[132:133], 0, s[40:41]
	global_load_dwordx2 v[186:187], v[132:133], off
	global_load_dwordx2 v[188:189], v[132:133], off offset:2048
	v_mfma_f32_16x16x32_bf16 v[62:65], v[238:241], v[222:225], v[62:65]
	v_mfma_f32_16x16x32_bf16 v[58:61], v[242:245], v[222:225], v[58:61]
	v_mfma_f32_16x16x32_bf16 v[54:57], v[246:249], v[222:225], v[54:57]
	v_mfma_f32_16x16x32_bf16 v[50:53], v[250:253], v[222:225], v[50:53]
	ds_read_b128 v[222:225], v93 offset:2048
	ds_read_b128 v[146:149], v141 offset:21504
	v_lshl_add_u64 v[166:167], v[132:133], 0, s[34:35]
	global_load_dwordx2 v[190:191], v[166:167], off
	global_load_dwordx2 v[192:193], v[166:167], off offset:2048
	v_mfma_f32_16x16x32_bf16 v[46:49], v[238:241], v[226:229], v[46:49]
	v_mfma_f32_16x16x32_bf16 v[42:45], v[242:245], v[226:229], v[42:45]
	v_mfma_f32_16x16x32_bf16 v[38:41], v[246:249], v[226:229], v[38:41]
	v_mfma_f32_16x16x32_bf16 v[34:37], v[250:253], v[226:229], v[34:37]
	ds_read_b128 v[226:229], v93 offset:4096
	ds_read_b128 v[150:153], v141 offset:23552
	v_lshl_add_u64 v[166:167], v[132:133], 0, s[36:37]
	global_load_dwordx2 v[194:195], v[166:167], off
	global_load_dwordx2 v[196:197], v[166:167], off offset:2048
	v_mfma_f32_16x16x32_bf16 v[18:21], v[238:241], v[230:233], v[18:21]
	v_mfma_f32_16x16x32_bf16 v[22:25], v[242:245], v[230:233], v[22:25]
	v_mfma_f32_16x16x32_bf16 v[26:29], v[246:249], v[230:233], v[26:29]
	v_mfma_f32_16x16x32_bf16 v[30:33], v[250:253], v[230:233], v[30:33]
	ds_read_b128 v[230:233], v93 offset:6144
	ds_read_b128 v[154:157], v141 offset:25600
	v_lshl_add_u64 v[166:167], v[132:133], 0, s[38:39]
	global_load_dwordx2 v[198:199], v[166:167], off
	global_load_dwordx2 v[200:201], v[166:167], off offset:2048
	v_mfma_f32_16x16x32_bf16 v[2:5], v[238:241], v[234:237], v[2:5]
	v_mfma_f32_16x16x32_bf16 v[6:9], v[242:245], v[234:237], v[6:9]
	v_mfma_f32_16x16x32_bf16 v[10:13], v[246:249], v[234:237], v[10:13]
	v_mfma_f32_16x16x32_bf16 v[14:17], v[250:253], v[234:237], v[14:17]
	ds_read_b128 v[234:237], v93 offset:8192
	s_waitcnt vmcnt(21)
	s_waitcnt lgkmcnt(0)
	s_barrier
; #define MU_GLDS_A(buf, kt) do { _Pragma("unroll") for (int i = 0; i < NMU; ++i) \
;         __builtin_amdgcn_global_load_lds((const unsigned*)((const char*)A + aoff[i] + (size_t)(kt) * 128), (PG8_LAS unsigned*)(MU_SA(buf) + wid * 1024 + i * 8192), 16, 0, 0); } while (0)
; #define MU_B_ISSUE(sb, kt) do { const char* kb_ = Bb + (size_t)(kt) * (64 * (size_t)RB); _Pragma("unroll") for (int j = 0; j < 8; ++j) { const char* p_ = kb_ + (size_t)j * RB; \
;         asm volatile("global_load_dwordx2 %0, %1, off" : "=&v"(sb[j]) : "v"(p_) : "memory"); } } while (0)
; #define MU_B_WAIT(sb, N) asm volatile("s_waitcnt vmcnt(%8)" : "+v"(sb[0]), "+v"(sb[1]), "+v"(sb[2]), "+v"(sb[3]), "+v"(sb[4]), "+v"(sb[5]), "+v"(sb[6]), "+v"(sb[7]) : "n"(N) : "memory")
; #define MU_COMPUTE(buf) MU_COMPUTE_N(buf, NMU)
; template <int MODE>
; __device__ __forceinline__ void moe_unit(PG8_LAS unsigned char* lds, int e, int cb, int slot0  , int nv  , const bf16_t* A, const int* slot_tok,
;                                          const float* W0, const float* W1, bf16_t* OUT, const float* slot_rs  , const int* slot_dst) {
;     ...
;     f32x4 acc[NMU][4];
; #pragma unroll
;     for (int m = 0; m < NMU; ++m)
; #pragma unroll
;         for (int n = 0; n < 4; ++n) acc[m][n] = (f32x4){0.f, 0.f, 0.f, 0.f};
;     f32x2 s0[8], s1[8];
;     float g0[8];
;     MU_GLDS_A(0, 0); MU_B_ISSUE(s0, 0); MU_G_LOAD(g0, 0); MU_B_ISSUE(s1, 1);
;     MU_B_WAIT(s0, 8); MU_B_WRITE(s0, 0, g0); __builtin_amdgcn_sched_barrier(0); MU_B_ISSUE(s0, 2);
;     asm volatile("s_waitcnt vmcnt(16)" ::: "memory");
;     asm volatile("s_waitcnt lgkmcnt(0)" ::: "memory"); __builtin_amdgcn_s_barrier(); asm volatile("" ::: "memory");
; #pragma unroll 1
;     for (int t = 0; t < nt; t += 2) {
;         if (t + 2 < nt) MU_B_WAIT(s1, 8); else MU_B_WAIT(s1, 0);
;         MU_G_LOAD(g0, t + 1); MU_B_WRITE(s1, 1, g0); __builtin_amdgcn_sched_barrier(0); MU_GLDS_A(1, t + 1); __builtin_amdgcn_sched_barrier(0);
;         if (t + 3 < nt) { MU_B_ISSUE(s1, t + 3); }
;         MU_COMPUTE(0);
;         MU_END(t + 3 >= nt);
;         if (t + 2 < nt) { MU_B_WAIT(s0, 8); MU_G_LOAD(g0, t + 2); MU_B_WRITE(s0, 0, g0); __builtin_amdgcn_sched_barrier(0); MU_GLDS_A(0, t + 2); __builtin_amdgcn_sched_barrier(0); }
;         if (t + 4 < nt) { MU_B_ISSUE(s0, t + 4); }
;         MU_COMPUTE(1);
;         MU_END(t + 4 >= nt);
	s_mov_b32 s47, s42
	s_mov_b32 s42, s43
	s_mov_b32 s43, s44
	s_mov_b32 s44, s47
	s_add_i32 s47, s44, s6
	s_add_u32 s30, s30, 0x80
	s_addc_u32 s31, s31, 0
	v_mfma_f32_16x16x32_bf16 v[78:81], v[142:145], v[218:221], v[78:81]
	v_mfma_f32_16x16x32_bf16 v[74:77], v[146:149], v[218:221], v[74:77]
	v_mfma_f32_16x16x32_bf16 v[70:73], v[150:153], v[218:221], v[70:73]
	v_mfma_f32_16x16x32_bf16 v[66:69], v[154:157], v[218:221], v[66:69]
	s_mov_b32 m0, s47
	s_nop 0
	global_load_lds_dwordx4 v86, s[30:31]
	v_mfma_f32_16x16x32_bf16 v[62:65], v[142:145], v[222:225], v[62:65]
	v_mfma_f32_16x16x32_bf16 v[58:61], v[146:149], v[222:225], v[58:61]
	v_mfma_f32_16x16x32_bf16 v[54:57], v[150:153], v[222:225], v[54:57]
	v_mfma_f32_16x16x32_bf16 v[50:53], v[154:157], v[222:225], v[50:53]
	s_add_i32 m0, s47, 0x2000
	s_nop 0
	global_load_lds_dwordx4 v134, s[30:31]
	v_mfma_f32_16x16x32_bf16 v[46:49], v[142:145], v[226:229], v[46:49]
	v_mfma_f32_16x16x32_bf16 v[42:45], v[146:149], v[226:229], v[42:45]
	v_mfma_f32_16x16x32_bf16 v[38:41], v[150:153], v[226:229], v[38:41]
	v_mfma_f32_16x16x32_bf16 v[34:37], v[154:157], v[226:229], v[34:37]
	s_add_i32 m0, s47, 0x4000
	s_nop 0
	global_load_lds_dwordx4 v136, s[30:31]
	v_mfma_f32_16x16x32_bf16 v[18:21], v[142:145], v[230:233], v[18:21]
	v_mfma_f32_16x16x32_bf16 v[22:25], v[146:149], v[230:233], v[22:25]
	v_mfma_f32_16x16x32_bf16 v[26:29], v[150:153], v[230:233], v[26:29]
	v_mfma_f32_16x16x32_bf16 v[30:33], v[154:157], v[230:233], v[30:33]
	s_add_i32 m0, s47, 0x6000
	s_nop 0
	global_load_lds_dwordx4 v138, s[30:31]
	v_mfma_f32_16x16x32_bf16 v[2:5], v[142:145], v[234:237], v[2:5]
	v_mfma_f32_16x16x32_bf16 v[6:9], v[146:149], v[234:237], v[6:9]
	v_mfma_f32_16x16x32_bf16 v[10:13], v[150:153], v[234:237], v[10:13]
	v_mfma_f32_16x16x32_bf16 v[14:17], v[154:157], v[234:237], v[14:17]
	s_add_i32 m0, s47, 0x8000
	s_nop 0
	global_load_lds_dwordx4 v140, s[30:31]
	v_mul_f32_e32 v202, s20, v202
	v_mul_f32_e32 v203, s20, v203
	v_mul_f32_e32 v204, s21, v204
	v_mul_f32_e32 v205, s21, v205
	v_mul_f32_e32 v206, s22, v206
	v_mul_f32_e32 v207, s22, v207
	v_mul_f32_e32 v208, s23, v208
	v_mul_f32_e32 v209, s23, v209
	v_mul_f32_e32 v210, s24, v210
	v_mul_f32_e32 v211, s24, v211
	v_mul_f32_e32 v212, s25, v212
	v_mul_f32_e32 v213, s25, v213
	v_mul_f32_e32 v214, s26, v214
	v_mul_f32_e32 v215, s26, v215
	v_mul_f32_e32 v216, s27, v216
	v_mul_f32_e32 v217, s27, v217
	v_cvt_pk_bf16_f32 v158, v202, v204
	v_cvt_pk_bf16_f32 v159, v206, v208
	v_cvt_pk_bf16_f32 v160, v210, v212
	v_cvt_pk_bf16_f32 v161, v214, v216
	v_cvt_pk_bf16_f32 v162, v203, v205
	v_cvt_pk_bf16_f32 v163, v207, v209
	v_cvt_pk_bf16_f32 v164, v211, v213
	v_cvt_pk_bf16_f32 v165, v215, v217
	ds_write_b128 v1, v[158:161] offset:19456
	ds_write_b128 v1, v[162:165] offset:19584
	v_add_u32_e32 v91, s42, v135
	v_add_u32_e32 v93, s42, v137
	ds_read_b128 v[238:241], v139 offset:0
	ds_read_b128 v[242:245], v139 offset:2048
	ds_read_b128 v[246:249], v139 offset:4096
	ds_read_b128 v[250:253], v139 offset:6144
	ds_read_b128 v[218:221], v91 offset:0
	ds_read_b128 v[222:225], v91 offset:2048
	ds_read_b128 v[226:229], v91 offset:4096
	ds_read_b128 v[230:233], v91 offset:6144
	ds_read_b128 v[234:237], v91 offset:8192
	s_waitcnt lgkmcnt(0)
	s_load_dwordx8 s[12:19], s[28:29], 0x0
	s_add_u32 s28, s28, 0x100
	s_addc_u32 s29, s29, 0
	v_mfma_f32_16x16x32_bf16 v[78:81], v[238:241], v[218:221], v[78:81]
	v_mfma_f32_16x16x32_bf16 v[74:77], v[242:245], v[218:221], v[74:77]
	v_mfma_f32_16x16x32_bf16 v[70:73], v[246:249], v[218:221], v[70:73]
	v_mfma_f32_16x16x32_bf16 v[66:69], v[250:253], v[218:221], v[66:69]
	ds_read_b128 v[218:221], v93 offset:0
	ds_read_b128 v[142:145], v141 offset:0
	v_lshl_add_u64 v[132:133], v[132:133], 0, s[40:41]
	global_load_dwordx2 v[202:203], v[132:133], off
	global_load_dwordx2 v[204:205], v[132:133], off offset:2048
	v_mfma_f32_16x16x32_bf16 v[62:65], v[238:241], v[222:225], v[62:65]
	v_mfma_f32_16x16x32_bf16 v[58:61], v[242:245], v[222:225], v[58:61]
	v_mfma_f32_16x16x32_bf16 v[54:57], v[246:249], v[222:225], v[54:57]
	v_mfma_f32_16x16x32_bf16 v[50:53], v[250:253], v[222:225], v[50:53]
	ds_read_b128 v[222:225], v93 offset:2048
	ds_read_b128 v[146:149], v141 offset:2048
	v_lshl_add_u64 v[166:167], v[132:133], 0, s[34:35]
	global_load_dwordx2 v[206:207], v[166:167], off
	global_load_dwordx2 v[208:209], v[166:167], off offset:2048
	v_mfma_f32_16x16x32_bf16 v[46:49], v[238:241], v[226:229], v[46:49]
	v_mfma_f32_16x16x32_bf16 v[42:45], v[242:245], v[226:229], v[42:45]
	v_mfma_f32_16x16x32_bf16 v[38:41], v[246:249], v[226:229], v[38:41]
	v_mfma_f32_16x16x32_bf16 v[34:37], v[250:253], v[226:229], v[34:37]
	ds_read_b128 v[226:229], v93 offset:4096
	ds_read_b128 v[150:153], v141 offset:4096
	v_lshl_add_u64 v[166:167], v[132:133], 0, s[36:37]
	global_load_dwordx2 v[210:211], v[166:167], off
	global_load_dwordx2 v[212:213], v[166:167], off offset:2048
	v_mfma_f32_16x16x32_bf16 v[18:21], v[238:241], v[230:233], v[18:21]
	v_mfma_f32_16x16x32_bf16 v[22:25], v[242:245], v[230:233], v[22:25]
	v_mfma_f32_16x16x32_bf16 v[26:29], v[246:249], v[230:233], v[26:29]
	v_mfma_f32_16x16x32_bf16 v[30:33], v[250:253], v[230:233], v[30:33]
	ds_read_b128 v[230:233], v93 offset:6144
	ds_read_b128 v[154:157], v141 offset:6144
	v_lshl_add_u64 v[166:167], v[132:133], 0, s[38:39]
	global_load_dwordx2 v[214:215], v[166:167], off
	global_load_dwordx2 v[216:217], v[166:167], off offset:2048
	v_mfma_f32_16x16x32_bf16 v[2:5], v[238:241], v[234:237], v[2:5]
	v_mfma_f32_16x16x32_bf16 v[6:9], v[242:245], v[234:237], v[6:9]
	v_mfma_f32_16x16x32_bf16 v[10:13], v[246:249], v[234:237], v[10:13]
	v_mfma_f32_16x16x32_bf16 v[14:17], v[250:253], v[234:237], v[14:17]
	ds_read_b128 v[234:237], v93 offset:8192
	s_waitcnt vmcnt(21)
	s_waitcnt lgkmcnt(0)
	s_barrier
; #define MU_GLDS_A(buf, kt) do { _Pragma("unroll") for (int i = 0; i < NMU; ++i) \
;         __builtin_amdgcn_global_load_lds((const unsigned*)((const char*)A + aoff[i] + (size_t)(kt) * 128), (PG8_LAS unsigned*)(MU_SA(buf) + wid * 1024 + i * 8192), 16, 0, 0); } while (0)
; #define MU_B_ISSUE(sb, kt) do { const char* kb_ = Bb + (size_t)(kt) * (64 * (size_t)RB); _Pragma("unroll") for (int j = 0; j < 8; ++j) { const char* p_ = kb_ + (size_t)j * RB; \
;         asm volatile("global_load_dwordx2 %0, %1, off" : "=&v"(sb[j]) : "v"(p_) : "memory"); } } while (0)
; #define MU_B_WAIT(sb, N) asm volatile("s_waitcnt vmcnt(%8)" : "+v"(sb[0]), "+v"(sb[1]), "+v"(sb[2]), "+v"(sb[3]), "+v"(sb[4]), "+v"(sb[5]), "+v"(sb[6]), "+v"(sb[7]) : "n"(N) : "memory")
; #define MU_COMPUTE(buf) MU_COMPUTE_N(buf, NMU)
; template <int MODE>
; __device__ __forceinline__ void moe_unit(PG8_LAS unsigned char* lds, int e, int cb, int slot0  , int nv  , const bf16_t* A, const int* slot_tok,
;                                          const float* W0, const float* W1, bf16_t* OUT, const float* slot_rs  , const int* slot_dst) {
;     ...
;     f32x4 acc[NMU][4];
; #pragma unroll
;     for (int m = 0; m < NMU; ++m)
; #pragma unroll
;         for (int n = 0; n < 4; ++n) acc[m][n] = (f32x4){0.f, 0.f, 0.f, 0.f};
;     f32x2 s0[8], s1[8];
;     float g0[8];
;     MU_GLDS_A(0, 0); MU_B_ISSUE(s0, 0); MU_G_LOAD(g0, 0); MU_B_ISSUE(s1, 1);
;     MU_B_WAIT(s0, 8); MU_B_WRITE(s0, 0, g0); __builtin_amdgcn_sched_barrier(0); MU_B_ISSUE(s0, 2);
;     asm volatile("s_waitcnt vmcnt(16)" ::: "memory");
;     asm volatile("s_waitcnt lgkmcnt(0)" ::: "memory"); __builtin_amdgcn_s_barrier(); asm volatile("" ::: "memory");
; #pragma unroll 1
;     for (int t = 0; t < nt; t += 2) {
;         if (t + 2 < nt) MU_B_WAIT(s1, 8); else MU_B_WAIT(s1, 0);
;         MU_G_LOAD(g0, t + 1); MU_B_WRITE(s1, 1, g0); __builtin_amdgcn_sched_barrier(0); MU_GLDS_A(1, t + 1); __builtin_amdgcn_sched_barrier(0);
;         if (t + 3 < nt) { MU_B_ISSUE(s1, t + 3); }
;         MU_COMPUTE(0);
;         MU_END(t + 3 >= nt);
;         if (t + 2 < nt) { MU_B_WAIT(s0, 8); MU_G_LOAD(g0, t + 2); MU_B_WRITE(s0, 0, g0); __builtin_amdgcn_sched_barrier(0); MU_GLDS_A(0, t + 2); __builtin_amdgcn_sched_barrier(0); }
;         if (t + 4 < nt) { MU_B_ISSUE(s0, t + 4); }
;         MU_COMPUTE(1);
;         MU_END(t + 4 >= nt);
	s_mov_b32 s47, s42
	s_mov_b32 s42, s43
	s_mov_b32 s43, s44
	s_mov_b32 s44, s47
	s_add_i32 s47, s44, s6
	s_add_u32 s30, s30, 0x80
	s_addc_u32 s31, s31, 0
	v_mfma_f32_16x16x32_bf16 v[78:81], v[142:145], v[218:221], v[78:81]
	v_mfma_f32_16x16x32_bf16 v[74:77], v[146:149], v[218:221], v[74:77]
	v_mfma_f32_16x16x32_bf16 v[70:73], v[150:153], v[218:221], v[70:73]
	v_mfma_f32_16x16x32_bf16 v[66:69], v[154:157], v[218:221], v[66:69]
	s_mov_b32 m0, s47
	s_nop 0
	global_load_lds_dwordx4 v86, s[30:31]
	v_mfma_f32_16x16x32_bf16 v[62:65], v[142:145], v[222:225], v[62:65]
	v_mfma_f32_16x16x32_bf16 v[58:61], v[146:149], v[222:225], v[58:61]
	v_mfma_f32_16x16x32_bf16 v[54:57], v[150:153], v[222:225], v[54:57]
	v_mfma_f32_16x16x32_bf16 v[50:53], v[154:157], v[222:225], v[50:53]
	s_add_i32 m0, s47, 0x2000
	s_nop 0
	global_load_lds_dwordx4 v134, s[30:31]
	v_mfma_f32_16x16x32_bf16 v[46:49], v[142:145], v[226:229], v[46:49]
	v_mfma_f32_16x16x32_bf16 v[42:45], v[146:149], v[226:229], v[42:45]
	v_mfma_f32_16x16x32_bf16 v[38:41], v[150:153], v[226:229], v[38:41]
	v_mfma_f32_16x16x32_bf16 v[34:37], v[154:157], v[226:229], v[34:37]
	s_add_i32 m0, s47, 0x4000
	s_nop 0
	global_load_lds_dwordx4 v136, s[30:31]
	v_mfma_f32_16x16x32_bf16 v[18:21], v[142:145], v[230:233], v[18:21]
	v_mfma_f32_16x16x32_bf16 v[22:25], v[146:149], v[230:233], v[22:25]
	v_mfma_f32_16x16x32_bf16 v[26:29], v[150:153], v[230:233], v[26:29]
	v_mfma_f32_16x16x32_bf16 v[30:33], v[154:157], v[230:233], v[30:33]
	s_add_i32 m0, s47, 0x6000
	s_nop 0
	global_load_lds_dwordx4 v138, s[30:31]
	v_mfma_f32_16x16x32_bf16 v[2:5], v[142:145], v[234:237], v[2:5]
	v_mfma_f32_16x16x32_bf16 v[6:9], v[146:149], v[234:237], v[6:9]
	v_mfma_f32_16x16x32_bf16 v[10:13], v[150:153], v[234:237], v[10:13]
	v_mfma_f32_16x16x32_bf16 v[14:17], v[154:157], v[234:237], v[14:17]
	s_add_i32 m0, s47, 0x8000
	s_nop 0
	global_load_lds_dwordx4 v140, s[30:31]
	v_mul_f32_e32 v98, s12, v98
	v_mul_f32_e32 v99, s12, v99
	v_mul_f32_e32 v100, s13, v100
	v_mul_f32_e32 v101, s13, v101
	v_mul_f32_e32 v102, s14, v102
	v_mul_f32_e32 v103, s14, v103
	v_mul_f32_e32 v104, s15, v104
	v_mul_f32_e32 v105, s15, v105
	v_mul_f32_e32 v106, s16, v106
	v_mul_f32_e32 v107, s16, v107
	v_mul_f32_e32 v108, s17, v108
	v_mul_f32_e32 v109, s17, v109
	v_mul_f32_e32 v110, s18, v110
	v_mul_f32_e32 v111, s18, v111
	v_mul_f32_e32 v112, s19, v112
	v_mul_f32_e32 v113, s19, v113
	v_cvt_pk_bf16_f32 v158, v98, v100
	v_cvt_pk_bf16_f32 v159, v102, v104
	v_cvt_pk_bf16_f32 v160, v106, v108
	v_cvt_pk_bf16_f32 v161, v110, v112
	v_cvt_pk_bf16_f32 v162, v99, v101
	v_cvt_pk_bf16_f32 v163, v103, v105
	v_cvt_pk_bf16_f32 v164, v107, v109
	v_cvt_pk_bf16_f32 v165, v111, v113
	ds_write_b128 v1, v[158:161] offset:0
	ds_write_b128 v1, v[162:165] offset:128
	v_add_u32_e32 v91, s42, v135
	v_add_u32_e32 v93, s42, v137
	ds_read_b128 v[238:241], v139 offset:19456
	ds_read_b128 v[242:245], v139 offset:21504
	ds_read_b128 v[246:249], v139 offset:23552
	ds_read_b128 v[250:253], v139 offset:25600
	ds_read_b128 v[218:221], v91 offset:0
	ds_read_b128 v[222:225], v91 offset:2048
	ds_read_b128 v[226:229], v91 offset:4096
	ds_read_b128 v[230:233], v91 offset:6144
	ds_read_b128 v[234:237], v91 offset:8192
	s_waitcnt lgkmcnt(0)
	s_load_dwordx8 s[20:27], s[28:29], 0x0
	s_add_u32 s28, s28, 0x100
	s_addc_u32 s29, s29, 0
	v_mfma_f32_16x16x32_bf16 v[78:81], v[238:241], v[218:221], v[78:81]
	v_mfma_f32_16x16x32_bf16 v[74:77], v[242:245], v[218:221], v[74:77]
	v_mfma_f32_16x16x32_bf16 v[70:73], v[246:249], v[218:221], v[70:73]
	v_mfma_f32_16x16x32_bf16 v[66:69], v[250:253], v[218:221], v[66:69]
	ds_read_b128 v[218:221], v93 offset:0
	ds_read_b128 v[142:145], v141 offset:19456
	v_lshl_add_u64 v[132:133], v[132:133], 0, s[40:41]
	global_load_dwordx2 v[98:99], v[132:133], off
	global_load_dwordx2 v[100:101], v[132:133], off offset:2048
	v_mfma_f32_16x16x32_bf16 v[62:65], v[238:241], v[222:225], v[62:65]
	v_mfma_f32_16x16x32_bf16 v[58:61], v[242:245], v[222:225], v[58:61]
	v_mfma_f32_16x16x32_bf16 v[54:57], v[246:249], v[222:225], v[54:57]
	v_mfma_f32_16x16x32_bf16 v[50:53], v[250:253], v[222:225], v[50:53]
	ds_read_b128 v[222:225], v93 offset:2048
	ds_read_b128 v[146:149], v141 offset:21504
	v_lshl_add_u64 v[166:167], v[132:133], 0, s[34:35]
	global_load_dwordx2 v[102:103], v[166:167], off
	global_load_dwordx2 v[104:105], v[166:167], off offset:2048
	v_mfma_f32_16x16x32_bf16 v[46:49], v[238:241], v[226:229], v[46:49]
	v_mfma_f32_16x16x32_bf16 v[42:45], v[242:245], v[226:229], v[42:45]
	v_mfma_f32_16x16x32_bf16 v[38:41], v[246:249], v[226:229], v[38:41]
	v_mfma_f32_16x16x32_bf16 v[34:37], v[250:253], v[226:229], v[34:37]
	ds_read_b128 v[226:229], v93 offset:4096
	ds_read_b128 v[150:153], v141 offset:23552
	v_lshl_add_u64 v[166:167], v[132:133], 0, s[36:37]
	global_load_dwordx2 v[106:107], v[166:167], off
	global_load_dwordx2 v[108:109], v[166:167], off offset:2048
	v_mfma_f32_16x16x32_bf16 v[18:21], v[238:241], v[230:233], v[18:21]
	v_mfma_f32_16x16x32_bf16 v[22:25], v[242:245], v[230:233], v[22:25]
	v_mfma_f32_16x16x32_bf16 v[26:29], v[246:249], v[230:233], v[26:29]
	v_mfma_f32_16x16x32_bf16 v[30:33], v[250:253], v[230:233], v[30:33]
	ds_read_b128 v[230:233], v93 offset:6144
	ds_read_b128 v[154:157], v141 offset:25600
	v_lshl_add_u64 v[166:167], v[132:133], 0, s[38:39]
	global_load_dwordx2 v[110:111], v[166:167], off
	global_load_dwordx2 v[112:113], v[166:167], off offset:2048
	v_mfma_f32_16x16x32_bf16 v[2:5], v[238:241], v[234:237], v[2:5]
	v_mfma_f32_16x16x32_bf16 v[6:9], v[242:245], v[234:237], v[6:9]
	v_mfma_f32_16x16x32_bf16 v[10:13], v[246:249], v[234:237], v[10:13]
	v_mfma_f32_16x16x32_bf16 v[14:17], v[250:253], v[234:237], v[14:17]
	ds_read_b128 v[234:237], v93 offset:8192
	s_waitcnt vmcnt(21)
	s_waitcnt lgkmcnt(0)
	s_barrier
	s_mov_b32 s47, s42
	s_mov_b32 s42, s43
	s_mov_b32 s43, s44
	s_mov_b32 s44, s47
	s_mov_b32 s46, 13

; #define MU_END(last) do { if (last) asm volatile("s_waitcnt vmcnt(0)" ::: "memory"); else asm volatile("s_waitcnt vmcnt(8)" ::: "memory"); \
;         asm volatile("s_waitcnt lgkmcnt(0)" ::: "memory"); __builtin_amdgcn_s_barrier(); asm volatile("" ::: "memory"); } while (0)
; template <int MODE>
; __device__ __forceinline__ void moe_unit(PG8_LAS unsigned char* lds, int e, int cb, int slot0  , int nv  , const bf16_t* A, const int* slot_tok,
;                                          const float* W0, const float* W1, bf16_t* OUT, const float* slot_rs  , const int* slot_dst) {
;     ...
;         MU_END(t + 4 >= nt);
;     }
; #pragma unroll
;     for (int m = 0; m < NMU; ++m) if (m < mcnt) { const int r = 4 * (16 * m + fr) + wr;
.Lmu_done:
	s_setprio 0


; #define MD_GLDS_A(buf, tau) do { _Pragma("unroll") for (int i = 0; i < 5; ++i) if (amask & (1u << i)) \
;         __builtin_amdgcn_global_load_lds((const unsigned*)((const char*)HIDp + aoff[i] + (size_t)((tau) & 7) * 128), (PG8_LAS unsigned*)(MD_SA(buf) + wid * 1024 + i * 8192), 16, 0, 0); } while (0)
; #define MD_B_ISSUE(sb, tau) do { const char* kb_ = Bb + (size_t)((tau) >> 3) * 512 + (size_t)((tau) & 7) * (64 * (size_t)RB); _Pragma("unroll") for (int j = 0; j < 8; ++j) { const char* p_ = kb_ + (size_t)j * RB; \
;         asm volatile("global_load_dwordx2 %0, %1, off" : "=&v"(sb[j]) : "v"(p_) : "memory"); } } while (0)
; #define MD_B_WAIT(sb, N) asm volatile("s_waitcnt vmcnt(%8)" : "+v"(sb[0]), "+v"(sb[1]), "+v"(sb[2]), "+v"(sb[3]), "+v"(sb[4]), "+v"(sb[5]), "+v"(sb[6]), "+v"(sb[7]) : "n"(N) : "memory")
; __device__ __forceinline__ void moe_down_stream(PG8_LAS unsigned char* lds, int e, int cb0, int slot0, int nv, const bf16_t* HIDp, const float* Wd, bf16_t* Y, const float* slot_w, const int* slot_dst) {
;     ...
;     f32x4 acc[DNM][4];
; #pragma unroll
;     for (int m = 0; m < DNM; ++m)
; #pragma unroll
;         for (int n = 0; n < 4; ++n) acc[m][n] = (f32x4){0.f, 0.f, 0.f, 0.f};
;     f32x2 s0[8], s1[8];
;     MD_GLDS_A(0, 0); MD_B_ISSUE(s0, 0); MD_B_ISSUE(s1, 1);
;     MD_B_WAIT(s0, 8); MD_B_WRITE(s0, 0); __builtin_amdgcn_sched_barrier(0); MD_B_ISSUE(s0, 2);
;     asm volatile("s_waitcnt vmcnt(16)" ::: "memory");
;     asm volatile("s_waitcnt lgkmcnt(0)" ::: "memory"); __builtin_amdgcn_s_barrier(); asm volatile("" ::: "memory");
; #pragma unroll 1
;     for (int t = 0; t < NT; t += 2) {
;         if (t + 2 < NT) MD_B_WAIT(s1, 8); else MD_B_WAIT(s1, 0);
;         MD_B_WRITE(s1, 1); __builtin_amdgcn_sched_barrier(0); MD_GLDS_A(1, t + 1); __builtin_amdgcn_sched_barrier(0);
;         if (t + 3 < NT) MD_B_ISSUE(s1, t + 3);
;         MD_COMPUTE(0);
;         MD_END(t + 3 >= NT);
;         if (t + 2 < NT) { MD_B_WAIT(s0, 8); MD_B_WRITE(s0, 0); __builtin_amdgcn_sched_barrier(0); MD_GLDS_A(0, t + 2); __builtin_amdgcn_sched_barrier(0); }
;         if (t + 4 < NT) MD_B_ISSUE(s0, t + 4);
;         MD_COMPUTE(1);
;         MD_END(t + 4 >= NT);
.Lmd_grpY:
	s_setprio 1
	s_add_i32 s49, s48, s74
	s_add_i32 s52, s52, 1
	s_and_b32 s54, s52, 7
	s_cmp_eq_u32 s54, 0
	s_cselect_b32 s54, s53, s32
	s_cselect_b32 s55, -1, 0
	s_add_u32 s30, s30, s54
	s_addc_u32 s31, s31, s55
	s_mov_b32 m0, s49
	s_nop 0
	global_load_lds_dwordx4 v88, s[30:31]
	s_add_i32 m0, s49, 0x2000
	s_nop 0
	global_load_lds_dwordx4 v90, s[30:31]
	s_add_i32 m0, s49, 0x4000
	s_nop 0
	global_load_lds_dwordx4 v92, s[30:31]
	s_add_i32 m0, s49, 0x6000
	s_nop 0
	global_load_lds_dwordx4 v94, s[30:31]
	s_add_i32 m0, s49, 0x8000
	s_nop 0
	global_load_lds_dwordx4 v96, s[30:31]
	s_waitcnt vmcnt(29)
	v_cvt_pk_bf16_f32 v172, v114, v116
	v_cvt_pk_bf16_f32 v173, v118, v120
	v_cvt_pk_bf16_f32 v174, v122, v124
	v_cvt_pk_bf16_f32 v175, v126, v128
	v_cvt_pk_bf16_f32 v176, v115, v117
	v_cvt_pk_bf16_f32 v177, v119, v121
	v_cvt_pk_bf16_f32 v178, v123, v125
	v_cvt_pk_bf16_f32 v179, v127, v129
	ds_write_b128 v95, v[172:175] offset:19456
	ds_write_b128 v95, v[176:179] offset:19584
	v_add_u32_e32 v91, s46, v135
	v_add_u32_e32 v93, s46, v137
	ds_read_b128 v[238:241], v139 offset:0
	ds_read_b128 v[242:245], v139 offset:2048
	ds_read_b128 v[246:249], v139 offset:4096
	ds_read_b128 v[250:253], v139 offset:6144
	ds_read_b128 v[218:221], v91 offset:0
	ds_read_b128 v[222:225], v91 offset:2048
	ds_read_b128 v[226:229], v91 offset:4096
	ds_read_b128 v[230:233], v91 offset:6144
	ds_read_b128 v[234:237], v91 offset:8192
	s_waitcnt lgkmcnt(0)
	v_mfma_f32_16x16x32_bf16 v[78:81], v[238:241], v[218:221], v[78:81]
	v_mfma_f32_16x16x32_bf16 v[74:77], v[242:245], v[218:221], v[74:77]
	v_mfma_f32_16x16x32_bf16 v[70:73], v[246:249], v[218:221], v[70:73]
	v_mfma_f32_16x16x32_bf16 v[66:69], v[250:253], v[218:221], v[66:69]
	ds_read_b128 v[218:221], v93 offset:0
	ds_read_b128 v[142:145], v141 offset:0
	s_add_i32 s51, s51, 1
	s_and_b32 s54, s51, 7
	s_cmp_eq_u32 s54, 0
	s_cselect_b32 s44, s34, s35
	s_cselect_b32 s45, -1, 0
	v_lshl_add_u64 v[132:133], v[132:133], 0, s[44:45]
	global_load_dwordx2 v[114:115], v[132:133], off
	v_lshl_add_u64 v[180:181], v[132:133], 0, s[24:25]
	global_load_dwordx2 v[116:117], v[180:181], off
	v_mfma_f32_16x16x32_bf16 v[62:65], v[238:241], v[222:225], v[62:65]
	v_mfma_f32_16x16x32_bf16 v[58:61], v[242:245], v[222:225], v[58:61]
	v_mfma_f32_16x16x32_bf16 v[54:57], v[246:249], v[222:225], v[54:57]
	v_mfma_f32_16x16x32_bf16 v[50:53], v[250:253], v[222:225], v[50:53]
	ds_read_b128 v[222:225], v93 offset:2048
	ds_read_b128 v[146:149], v141 offset:2048
	v_lshl_add_u64 v[180:181], v[132:133], 0, s[26:27]
	global_load_dwordx2 v[118:119], v[180:181], off
	v_lshl_add_u64 v[180:181], v[132:133], 0, s[28:29]
	global_load_dwordx2 v[120:121], v[180:181], off
	v_mfma_f32_16x16x32_bf16 v[46:49], v[238:241], v[226:229], v[46:49]
	v_mfma_f32_16x16x32_bf16 v[42:45], v[242:245], v[226:229], v[42:45]
	v_mfma_f32_16x16x32_bf16 v[38:41], v[246:249], v[226:229], v[38:41]
	v_mfma_f32_16x16x32_bf16 v[34:37], v[250:253], v[226:229], v[34:37]
	ds_read_b128 v[226:229], v93 offset:4096
	ds_read_b128 v[156:159], v141 offset:4096
	v_lshl_add_u64 v[180:181], v[132:133], 0, s[36:37]
	global_load_dwordx2 v[122:123], v[180:181], off
	v_lshl_add_u64 v[180:181], v[132:133], 0, s[38:39]
	global_load_dwordx2 v[124:125], v[180:181], off
	v_mfma_f32_16x16x32_bf16 v[18:21], v[238:241], v[230:233], v[18:21]
	v_mfma_f32_16x16x32_bf16 v[22:25], v[242:245], v[230:233], v[22:25]
	v_mfma_f32_16x16x32_bf16 v[26:29], v[246:249], v[230:233], v[26:29]
	v_mfma_f32_16x16x32_bf16 v[30:33], v[250:253], v[230:233], v[30:33]
	ds_read_b128 v[230:233], v93 offset:6144
	ds_read_b128 v[160:163], v141 offset:6144
	v_lshl_add_u64 v[180:181], v[132:133], 0, s[40:41]
	global_load_dwordx2 v[126:127], v[180:181], off
	v_lshl_add_u64 v[180:181], v[132:133], 0, s[42:43]
	global_load_dwordx2 v[128:129], v[180:181], off
	v_mfma_f32_16x16x32_bf16 v[2:5], v[238:241], v[234:237], v[2:5]
	v_mfma_f32_16x16x32_bf16 v[6:9], v[242:245], v[234:237], v[6:9]
	v_mfma_f32_16x16x32_bf16 v[10:13], v[246:249], v[234:237], v[10:13]
	v_mfma_f32_16x16x32_bf16 v[14:17], v[250:253], v[234:237], v[14:17]
	ds_read_b128 v[234:237], v93 offset:8192
	s_waitcnt lgkmcnt(0)
	s_barrier
	s_mov_b32 s49, s46
	s_mov_b32 s46, s47
	s_mov_b32 s47, s48
	s_mov_b32 s48, s49
	s_add_i32 s50, s50, 1
	s_add_i32 s49, s48, s74
	s_add_i32 s52, s52, 1
	s_and_b32 s54, s52, 7
	s_cmp_eq_u32 s54, 0
	s_cselect_b32 s54, s53, s32
	s_cselect_b32 s55, -1, 0
	s_add_u32 s30, s30, s54
	s_addc_u32 s31, s31, s55
	v_mfma_f32_16x16x32_bf16 v[78:81], v[142:145], v[218:221], v[78:81]
	v_mfma_f32_16x16x32_bf16 v[74:77], v[146:149], v[218:221], v[74:77]
	v_mfma_f32_16x16x32_bf16 v[70:73], v[156:159], v[218:221], v[70:73]
	v_mfma_f32_16x16x32_bf16 v[66:69], v[160:163], v[218:221], v[66:69]
	s_mov_b32 m0, s49
	s_nop 0
	global_load_lds_dwordx4 v88, s[30:31]
	v_mfma_f32_16x16x32_bf16 v[62:65], v[142:145], v[222:225], v[62:65]
	v_mfma_f32_16x16x32_bf16 v[58:61], v[146:149], v[222:225], v[58:61]
	v_mfma_f32_16x16x32_bf16 v[54:57], v[156:159], v[222:225], v[54:57]
	v_mfma_f32_16x16x32_bf16 v[50:53], v[160:163], v[222:225], v[50:53]
	s_add_i32 m0, s49, 0x2000
	s_nop 0
	global_load_lds_dwordx4 v90, s[30:31]
	v_mfma_f32_16x16x32_bf16 v[46:49], v[142:145], v[226:229], v[46:49]
	v_mfma_f32_16x16x32_bf16 v[42:45], v[146:149], v[226:229], v[42:45]
	v_mfma_f32_16x16x32_bf16 v[38:41], v[156:159], v[226:229], v[38:41]
	v_mfma_f32_16x16x32_bf16 v[34:37], v[160:163], v[226:229], v[34:37]
	s_add_i32 m0, s49, 0x4000
	s_nop 0
	global_load_lds_dwordx4 v92, s[30:31]
	v_mfma_f32_16x16x32_bf16 v[18:21], v[142:145], v[230:233], v[18:21]
	v_mfma_f32_16x16x32_bf16 v[22:25], v[146:149], v[230:233], v[22:25]
	v_mfma_f32_16x16x32_bf16 v[26:29], v[156:159], v[230:233], v[26:29]
	v_mfma_f32_16x16x32_bf16 v[30:33], v[160:163], v[230:233], v[30:33]
	s_add_i32 m0, s49, 0x6000
	s_nop 0
	global_load_lds_dwordx4 v94, s[30:31]
	v_mfma_f32_16x16x32_bf16 v[2:5], v[142:145], v[234:237], v[2:5]
	v_mfma_f32_16x16x32_bf16 v[6:9], v[146:149], v[234:237], v[6:9]
	v_mfma_f32_16x16x32_bf16 v[10:13], v[156:159], v[234:237], v[10:13]
	v_mfma_f32_16x16x32_bf16 v[14:17], v[160:163], v[234:237], v[14:17]
	s_add_i32 m0, s49, 0x8000
	s_nop 0
	global_load_lds_dwordx4 v96, s[30:31]
	s_waitcnt vmcnt(34)
; #define MD_GLDS_A(buf, tau) do { _Pragma("unroll") for (int i = 0; i < 5; ++i) if (amask & (1u << i)) \
;         __builtin_amdgcn_global_load_lds((const unsigned*)((const char*)HIDp + aoff[i] + (size_t)((tau) & 7) * 128), (PG8_LAS unsigned*)(MD_SA(buf) + wid * 1024 + i * 8192), 16, 0, 0); } while (0)
; #define MD_B_ISSUE(sb, tau) do { const char* kb_ = Bb + (size_t)((tau) >> 3) * 512 + (size_t)((tau) & 7) * (64 * (size_t)RB); _Pragma("unroll") for (int j = 0; j < 8; ++j) { const char* p_ = kb_ + (size_t)j * RB; \
;         asm volatile("global_load_dwordx2 %0, %1, off" : "=&v"(sb[j]) : "v"(p_) : "memory"); } } while (0)
; #define MD_B_WAIT(sb, N) asm volatile("s_waitcnt vmcnt(%8)" : "+v"(sb[0]), "+v"(sb[1]), "+v"(sb[2]), "+v"(sb[3]), "+v"(sb[4]), "+v"(sb[5]), "+v"(sb[6]), "+v"(sb[7]) : "n"(N) : "memory")
; __device__ __forceinline__ void moe_down_stream(PG8_LAS unsigned char* lds, int e, int cb0, int slot0, int nv, const bf16_t* HIDp, const float* Wd, bf16_t* Y, const float* slot_w, const int* slot_dst) {
;     ...
;     f32x4 acc[DNM][4];
; #pragma unroll
;     for (int m = 0; m < DNM; ++m)
; #pragma unroll
;         for (int n = 0; n < 4; ++n) acc[m][n] = (f32x4){0.f, 0.f, 0.f, 0.f};
;     f32x2 s0[8], s1[8];
;     MD_GLDS_A(0, 0); MD_B_ISSUE(s0, 0); MD_B_ISSUE(s1, 1);
;     MD_B_WAIT(s0, 8); MD_B_WRITE(s0, 0); __builtin_amdgcn_sched_barrier(0); MD_B_ISSUE(s0, 2);
;     asm volatile("s_waitcnt vmcnt(16)" ::: "memory");
;     asm volatile("s_waitcnt lgkmcnt(0)" ::: "memory"); __builtin_amdgcn_s_barrier(); asm volatile("" ::: "memory");
; #pragma unroll 1
;     for (int t = 0; t < NT; t += 2) {
;         if (t + 2 < NT) MD_B_WAIT(s1, 8); else MD_B_WAIT(s1, 0);
;         MD_B_WRITE(s1, 1); __builtin_amdgcn_sched_barrier(0); MD_GLDS_A(1, t + 1); __builtin_amdgcn_sched_barrier(0);
;         if (t + 3 < NT) MD_B_ISSUE(s1, t + 3);
;         MD_COMPUTE(0);
;         MD_END(t + 3 >= NT);
;         if (t + 2 < NT) { MD_B_WAIT(s0, 8); MD_B_WRITE(s0, 0); __builtin_amdgcn_sched_barrier(0); MD_GLDS_A(0, t + 2); __builtin_amdgcn_sched_barrier(0); }
;         if (t + 4 < NT) MD_B_ISSUE(s0, t + 4);
;         MD_COMPUTE(1);
;         MD_END(t + 4 >= NT);
	v_cvt_pk_bf16_f32 v172, v186, v188
	v_cvt_pk_bf16_f32 v173, v190, v192
	v_cvt_pk_bf16_f32 v174, v194, v196
	v_cvt_pk_bf16_f32 v175, v198, v200
	v_cvt_pk_bf16_f32 v176, v187, v189
	v_cvt_pk_bf16_f32 v177, v191, v193
	v_cvt_pk_bf16_f32 v178, v195, v197
	v_cvt_pk_bf16_f32 v179, v199, v201
	ds_write_b128 v95, v[172:175] offset:0
	ds_write_b128 v95, v[176:179] offset:128
	v_add_u32_e32 v91, s46, v135
	v_add_u32_e32 v93, s46, v137
	ds_read_b128 v[238:241], v139 offset:19456
	ds_read_b128 v[242:245], v139 offset:21504
	ds_read_b128 v[246:249], v139 offset:23552
	ds_read_b128 v[250:253], v139 offset:25600
	ds_read_b128 v[218:221], v91 offset:0
	ds_read_b128 v[222:225], v91 offset:2048
	ds_read_b128 v[226:229], v91 offset:4096
	ds_read_b128 v[230:233], v91 offset:6144
	ds_read_b128 v[234:237], v91 offset:8192
	s_waitcnt lgkmcnt(0)
	v_mfma_f32_16x16x32_bf16 v[78:81], v[238:241], v[218:221], v[78:81]
	v_mfma_f32_16x16x32_bf16 v[74:77], v[242:245], v[218:221], v[74:77]
	v_mfma_f32_16x16x32_bf16 v[70:73], v[246:249], v[218:221], v[70:73]
	v_mfma_f32_16x16x32_bf16 v[66:69], v[250:253], v[218:221], v[66:69]
	ds_read_b128 v[218:221], v93 offset:0
	ds_read_b128 v[142:145], v141 offset:19456
	s_add_i32 s51, s51, 1
	s_and_b32 s54, s51, 7
	s_cmp_eq_u32 s54, 0
	s_cselect_b32 s44, s34, s35
	s_cselect_b32 s45, -1, 0
	v_lshl_add_u64 v[132:133], v[132:133], 0, s[44:45]
	global_load_dwordx2 v[186:187], v[132:133], off
	v_lshl_add_u64 v[180:181], v[132:133], 0, s[24:25]
	global_load_dwordx2 v[188:189], v[180:181], off
	v_mfma_f32_16x16x32_bf16 v[62:65], v[238:241], v[222:225], v[62:65]
	v_mfma_f32_16x16x32_bf16 v[58:61], v[242:245], v[222:225], v[58:61]
	v_mfma_f32_16x16x32_bf16 v[54:57], v[246:249], v[222:225], v[54:57]
	v_mfma_f32_16x16x32_bf16 v[50:53], v[250:253], v[222:225], v[50:53]
	ds_read_b128 v[222:225], v93 offset:2048
	ds_read_b128 v[146:149], v141 offset:21504
	v_lshl_add_u64 v[180:181], v[132:133], 0, s[26:27]
	global_load_dwordx2 v[190:191], v[180:181], off
	v_lshl_add_u64 v[180:181], v[132:133], 0, s[28:29]
	global_load_dwordx2 v[192:193], v[180:181], off
	v_mfma_f32_16x16x32_bf16 v[46:49], v[238:241], v[226:229], v[46:49]
	v_mfma_f32_16x16x32_bf16 v[42:45], v[242:245], v[226:229], v[42:45]
	v_mfma_f32_16x16x32_bf16 v[38:41], v[246:249], v[226:229], v[38:41]
	v_mfma_f32_16x16x32_bf16 v[34:37], v[250:253], v[226:229], v[34:37]
	ds_read_b128 v[226:229], v93 offset:4096
	ds_read_b128 v[156:159], v141 offset:23552
	v_lshl_add_u64 v[180:181], v[132:133], 0, s[36:37]
	global_load_dwordx2 v[194:195], v[180:181], off
	v_lshl_add_u64 v[180:181], v[132:133], 0, s[38:39]
	global_load_dwordx2 v[196:197], v[180:181], off
	v_mfma_f32_16x16x32_bf16 v[18:21], v[238:241], v[230:233], v[18:21]
	v_mfma_f32_16x16x32_bf16 v[22:25], v[242:245], v[230:233], v[22:25]
	v_mfma_f32_16x16x32_bf16 v[26:29], v[246:249], v[230:233], v[26:29]
	v_mfma_f32_16x16x32_bf16 v[30:33], v[250:253], v[230:233], v[30:33]
	ds_read_b128 v[230:233], v93 offset:6144
	ds_read_b128 v[160:163], v141 offset:25600
	v_lshl_add_u64 v[180:181], v[132:133], 0, s[40:41]
	global_load_dwordx2 v[198:199], v[180:181], off
	v_lshl_add_u64 v[180:181], v[132:133], 0, s[42:43]
	global_load_dwordx2 v[200:201], v[180:181], off
	v_mfma_f32_16x16x32_bf16 v[2:5], v[238:241], v[234:237], v[2:5]
	v_mfma_f32_16x16x32_bf16 v[6:9], v[242:245], v[234:237], v[6:9]
	v_mfma_f32_16x16x32_bf16 v[10:13], v[246:249], v[234:237], v[10:13]
	v_mfma_f32_16x16x32_bf16 v[14:17], v[250:253], v[234:237], v[14:17]
	ds_read_b128 v[234:237], v93 offset:8192
	s_waitcnt vmcnt(21)
	s_waitcnt lgkmcnt(0)
	s_barrier
	s_mov_b32 s49, s46
	s_mov_b32 s46, s47
	s_mov_b32 s47, s48
	s_mov_b32 s48, s49
	s_add_i32 s50, s50, 1
	s_add_i32 s49, s48, s74
	s_add_i32 s52, s52, 1
	s_and_b32 s54, s52, 7
	s_cmp_eq_u32 s54, 0
	s_cselect_b32 s54, s53, s32
	s_cselect_b32 s55, -1, 0
	s_add_u32 s30, s30, s54
	s_addc_u32 s31, s31, s55
	v_mfma_f32_16x16x32_bf16 v[78:81], v[142:145], v[218:221], v[78:81]
	v_mfma_f32_16x16x32_bf16 v[74:77], v[146:149], v[218:221], v[74:77]
	v_mfma_f32_16x16x32_bf16 v[70:73], v[156:159], v[218:221], v[70:73]
	v_mfma_f32_16x16x32_bf16 v[66:69], v[160:163], v[218:221], v[66:69]
	s_mov_b32 m0, s49
	s_nop 0
	global_load_lds_dwordx4 v88, s[30:31]
	v_mfma_f32_16x16x32_bf16 v[62:65], v[142:145], v[222:225], v[62:65]
	v_mfma_f32_16x16x32_bf16 v[58:61], v[146:149], v[222:225], v[58:61]
	v_mfma_f32_16x16x32_bf16 v[54:57], v[156:159], v[222:225], v[54:57]
	v_mfma_f32_16x16x32_bf16 v[50:53], v[160:163], v[222:225], v[50:53]
	s_add_i32 m0, s49, 0x2000
	s_nop 0
	global_load_lds_dwordx4 v90, s[30:31]
	v_mfma_f32_16x16x32_bf16 v[46:49], v[142:145], v[226:229], v[46:49]
	v_mfma_f32_16x16x32_bf16 v[42:45], v[146:149], v[226:229], v[42:45]
	v_mfma_f32_16x16x32_bf16 v[38:41], v[156:159], v[226:229], v[38:41]
	v_mfma_f32_16x16x32_bf16 v[34:37], v[160:163], v[226:229], v[34:37]
	s_add_i32 m0, s49, 0x4000
	s_nop 0
	global_load_lds_dwordx4 v92, s[30:31]
	v_mfma_f32_16x16x32_bf16 v[18:21], v[142:145], v[230:233], v[18:21]
	v_mfma_f32_16x16x32_bf16 v[22:25], v[146:149], v[230:233], v[22:25]
	v_mfma_f32_16x16x32_bf16 v[26:29], v[156:159], v[230:233], v[26:29]
	v_mfma_f32_16x16x32_bf16 v[30:33], v[160:163], v[230:233], v[30:33]
	s_add_i32 m0, s49, 0x6000
	s_nop 0
	global_load_lds_dwordx4 v94, s[30:31]
	v_mfma_f32_16x16x32_bf16 v[2:5], v[142:145], v[234:237], v[2:5]
	v_mfma_f32_16x16x32_bf16 v[6:9], v[146:149], v[234:237], v[6:9]
	v_mfma_f32_16x16x32_bf16 v[10:13], v[156:159], v[234:237], v[10:13]
	v_mfma_f32_16x16x32_bf16 v[14:17], v[160:163], v[234:237], v[14:17]
	s_add_i32 m0, s49, 0x8000
	s_nop 0
	global_load_lds_dwordx4 v96, s[30:31]
	v_cvt_pk_bf16_f32 v172, v202, v204
	v_cvt_pk_bf16_f32 v173, v206, v208
	v_cvt_pk_bf16_f32 v174, v210, v212
	v_cvt_pk_bf16_f32 v175, v214, v216
	v_cvt_pk_bf16_f32 v176, v203, v205
	v_cvt_pk_bf16_f32 v177, v207, v209
	v_cvt_pk_bf16_f32 v178, v211, v213
	v_cvt_pk_bf16_f32 v179, v215, v217
	ds_write_b128 v95, v[172:175] offset:19456
	ds_write_b128 v95, v[176:179] offset:19584
	v_add_u32_e32 v91, s46, v135
	v_add_u32_e32 v93, s46, v137
	ds_read_b128 v[238:241], v139 offset:0
	ds_read_b128 v[242:245], v139 offset:2048
	ds_read_b128 v[246:249], v139 offset:4096
	ds_read_b128 v[250:253], v139 offset:6144
	ds_read_b128 v[218:221], v91 offset:0
	ds_read_b128 v[222:225], v91 offset:2048
	ds_read_b128 v[226:229], v91 offset:4096
	ds_read_b128 v[230:233], v91 offset:6144
	ds_read_b128 v[234:237], v91 offset:8192
	s_waitcnt lgkmcnt(0)
; #define MD_GLDS_A(buf, tau) do { _Pragma("unroll") for (int i = 0; i < 5; ++i) if (amask & (1u << i)) \
;         __builtin_amdgcn_global_load_lds((const unsigned*)((const char*)HIDp + aoff[i] + (size_t)((tau) & 7) * 128), (PG8_LAS unsigned*)(MD_SA(buf) + wid * 1024 + i * 8192), 16, 0, 0); } while (0)
; #define MD_B_ISSUE(sb, tau) do { const char* kb_ = Bb + (size_t)((tau) >> 3) * 512 + (size_t)((tau) & 7) * (64 * (size_t)RB); _Pragma("unroll") for (int j = 0; j < 8; ++j) { const char* p_ = kb_ + (size_t)j * RB; \
;         asm volatile("global_load_dwordx2 %0, %1, off" : "=&v"(sb[j]) : "v"(p_) : "memory"); } } while (0)
; #define MD_B_WAIT(sb, N) asm volatile("s_waitcnt vmcnt(%8)" : "+v"(sb[0]), "+v"(sb[1]), "+v"(sb[2]), "+v"(sb[3]), "+v"(sb[4]), "+v"(sb[5]), "+v"(sb[6]), "+v"(sb[7]) : "n"(N) : "memory")
; #define MD_END(last) do { if (last) asm volatile("s_waitcnt vmcnt(0)" ::: "memory"); else asm volatile("s_waitcnt vmcnt(8)" ::: "memory"); \
;         asm volatile("s_waitcnt lgkmcnt(0)" ::: "memory"); __builtin_amdgcn_s_barrier(); asm volatile("" ::: "memory"); } while (0)
; __device__ __forceinline__ void moe_down_stream(PG8_LAS unsigned char* lds, int e, int cb0, int slot0, int nv, const bf16_t* HIDp, const float* Wd, bf16_t* Y, const float* slot_w, const int* slot_dst) {
;     ...
;     f32x4 acc[DNM][4];
; #pragma unroll
;     for (int m = 0; m < DNM; ++m)
; #pragma unroll
;         for (int n = 0; n < 4; ++n) acc[m][n] = (f32x4){0.f, 0.f, 0.f, 0.f};
;     f32x2 s0[8], s1[8];
;     MD_GLDS_A(0, 0); MD_B_ISSUE(s0, 0); MD_B_ISSUE(s1, 1);
;     MD_B_WAIT(s0, 8); MD_B_WRITE(s0, 0); __builtin_amdgcn_sched_barrier(0); MD_B_ISSUE(s0, 2);
;     asm volatile("s_waitcnt vmcnt(16)" ::: "memory");
;     asm volatile("s_waitcnt lgkmcnt(0)" ::: "memory"); __builtin_amdgcn_s_barrier(); asm volatile("" ::: "memory");
; #pragma unroll 1
;     for (int t = 0; t < NT; t += 2) {
;         if (t + 2 < NT) MD_B_WAIT(s1, 8); else MD_B_WAIT(s1, 0);
;         MD_B_WRITE(s1, 1); __builtin_amdgcn_sched_barrier(0); MD_GLDS_A(1, t + 1); __builtin_amdgcn_sched_barrier(0);
;         if (t + 3 < NT) MD_B_ISSUE(s1, t + 3);
;         MD_COMPUTE(0);
;         MD_END(t + 3 >= NT);
	v_mfma_f32_16x16x32_bf16 v[78:81], v[238:241], v[218:221], v[78:81]
	v_mfma_f32_16x16x32_bf16 v[74:77], v[242:245], v[218:221], v[74:77]
	v_mfma_f32_16x16x32_bf16 v[70:73], v[246:249], v[218:221], v[70:73]
	v_mfma_f32_16x16x32_bf16 v[66:69], v[250:253], v[218:221], v[66:69]
	ds_read_b128 v[218:221], v93 offset:0
	ds_read_b128 v[142:145], v141 offset:0
	s_add_i32 s51, s51, 1
	s_and_b32 s54, s51, 7
	s_cmp_eq_u32 s54, 0
	s_cselect_b32 s44, s34, s35
	s_cselect_b32 s45, -1, 0
	v_lshl_add_u64 v[132:133], v[132:133], 0, s[44:45]
	global_load_dwordx2 v[202:203], v[132:133], off
	v_lshl_add_u64 v[180:181], v[132:133], 0, s[24:25]
	global_load_dwordx2 v[204:205], v[180:181], off
	v_mfma_f32_16x16x32_bf16 v[62:65], v[238:241], v[222:225], v[62:65]
	v_mfma_f32_16x16x32_bf16 v[58:61], v[242:245], v[222:225], v[58:61]
	v_mfma_f32_16x16x32_bf16 v[54:57], v[246:249], v[222:225], v[54:57]
	v_mfma_f32_16x16x32_bf16 v[50:53], v[250:253], v[222:225], v[50:53]
	ds_read_b128 v[222:225], v93 offset:2048
	ds_read_b128 v[146:149], v141 offset:2048
	v_lshl_add_u64 v[180:181], v[132:133], 0, s[26:27]
	global_load_dwordx2 v[206:207], v[180:181], off
	v_lshl_add_u64 v[180:181], v[132:133], 0, s[28:29]
	global_load_dwordx2 v[208:209], v[180:181], off
	v_mfma_f32_16x16x32_bf16 v[46:49], v[238:241], v[226:229], v[46:49]
	v_mfma_f32_16x16x32_bf16 v[42:45], v[242:245], v[226:229], v[42:45]
	v_mfma_f32_16x16x32_bf16 v[38:41], v[246:249], v[226:229], v[38:41]
	v_mfma_f32_16x16x32_bf16 v[34:37], v[250:253], v[226:229], v[34:37]
	ds_read_b128 v[226:229], v93 offset:4096
	ds_read_b128 v[156:159], v141 offset:4096
	v_lshl_add_u64 v[180:181], v[132:133], 0, s[36:37]
	global_load_dwordx2 v[210:211], v[180:181], off
	v_lshl_add_u64 v[180:181], v[132:133], 0, s[38:39]
	global_load_dwordx2 v[212:213], v[180:181], off
	v_mfma_f32_16x16x32_bf16 v[18:21], v[238:241], v[230:233], v[18:21]
	v_mfma_f32_16x16x32_bf16 v[22:25], v[242:245], v[230:233], v[22:25]
	v_mfma_f32_16x16x32_bf16 v[26:29], v[246:249], v[230:233], v[26:29]
	v_mfma_f32_16x16x32_bf16 v[30:33], v[250:253], v[230:233], v[30:33]
	ds_read_b128 v[230:233], v93 offset:6144
	ds_read_b128 v[160:163], v141 offset:6144
	v_lshl_add_u64 v[180:181], v[132:133], 0, s[40:41]
	global_load_dwordx2 v[214:215], v[180:181], off
	v_lshl_add_u64 v[180:181], v[132:133], 0, s[42:43]
	global_load_dwordx2 v[216:217], v[180:181], off
	v_mfma_f32_16x16x32_bf16 v[2:5], v[238:241], v[234:237], v[2:5]
	v_mfma_f32_16x16x32_bf16 v[6:9], v[242:245], v[234:237], v[6:9]
	v_mfma_f32_16x16x32_bf16 v[10:13], v[246:249], v[234:237], v[10:13]
	v_mfma_f32_16x16x32_bf16 v[14:17], v[250:253], v[234:237], v[14:17]
	ds_read_b128 v[234:237], v93 offset:8192
	s_waitcnt vmcnt(21)
	s_waitcnt lgkmcnt(0)
	s_barrier
; #define MD_GLDS_A(buf, tau) do { _Pragma("unroll") for (int i = 0; i < 5; ++i) if (amask & (1u << i)) \
;         __builtin_amdgcn_global_load_lds((const unsigned*)((const char*)HIDp + aoff[i] + (size_t)((tau) & 7) * 128), (PG8_LAS unsigned*)(MD_SA(buf) + wid * 1024 + i * 8192), 16, 0, 0); } while (0)
; #define MD_B_ISSUE(sb, tau) do { const char* kb_ = Bb + (size_t)((tau) >> 3) * 512 + (size_t)((tau) & 7) * (64 * (size_t)RB); _Pragma("unroll") for (int j = 0; j < 8; ++j) { const char* p_ = kb_ + (size_t)j * RB; \
;         asm volatile("global_load_dwordx2 %0, %1, off" : "=&v"(sb[j]) : "v"(p_) : "memory"); } } while (0)
; #define MD_B_WAIT(sb, N) asm volatile("s_waitcnt vmcnt(%8)" : "+v"(sb[0]), "+v"(sb[1]), "+v"(sb[2]), "+v"(sb[3]), "+v"(sb[4]), "+v"(sb[5]), "+v"(sb[6]), "+v"(sb[7]) : "n"(N) : "memory")
; #define MD_END(last) do { if (last) asm volatile("s_waitcnt vmcnt(0)" ::: "memory"); else asm volatile("s_waitcnt vmcnt(8)" ::: "memory"); \
;         asm volatile("s_waitcnt lgkmcnt(0)" ::: "memory"); __builtin_amdgcn_s_barrier(); asm volatile("" ::: "memory"); } while (0)
; __device__ __forceinline__ void moe_down_stream(PG8_LAS unsigned char* lds, int e, int cb0, int slot0, int nv, const bf16_t* HIDp, const float* Wd, bf16_t* Y, const float* slot_w, const int* slot_dst) {
;     ...
;     for (int t = 0; t < NT; t += 2) {
;         if (t + 2 < NT) MD_B_WAIT(s1, 8); else MD_B_WAIT(s1, 0);
;         MD_B_WRITE(s1, 1); __builtin_amdgcn_sched_barrier(0); MD_GLDS_A(1, t + 1); __builtin_amdgcn_sched_barrier(0);
;         if (t + 3 < NT) MD_B_ISSUE(s1, t + 3);
;         MD_COMPUTE(0);
;         MD_END(t + 3 >= NT);
;         if (t + 2 < NT) { MD_B_WAIT(s0, 8); MD_B_WRITE(s0, 0); __builtin_amdgcn_sched_barrier(0); MD_GLDS_A(0, t + 2); __builtin_amdgcn_sched_barrier(0); }
;         if (t + 4 < NT) MD_B_ISSUE(s0, t + 4);
;         MD_COMPUTE(1);
;         MD_END(t + 4 >= NT);
	s_mov_b32 s49, s46
	s_mov_b32 s46, s47
	s_mov_b32 s47, s48
	s_mov_b32 s48, s49
	s_add_i32 s50, s50, 1
	s_add_i32 s49, s48, s74
	s_add_i32 s52, s52, 1
	s_and_b32 s54, s52, 7
	s_cmp_eq_u32 s54, 0
	s_cselect_b32 s54, s53, s32
	s_cselect_b32 s55, -1, 0
	s_add_u32 s30, s30, s54
	s_addc_u32 s31, s31, s55
	v_mfma_f32_16x16x32_bf16 v[78:81], v[142:145], v[218:221], v[78:81]
	v_mfma_f32_16x16x32_bf16 v[74:77], v[146:149], v[218:221], v[74:77]
	v_mfma_f32_16x16x32_bf16 v[70:73], v[156:159], v[218:221], v[70:73]
	v_mfma_f32_16x16x32_bf16 v[66:69], v[160:163], v[218:221], v[66:69]
	s_mov_b32 m0, s49
	s_nop 0
	global_load_lds_dwordx4 v88, s[30:31]
	v_mfma_f32_16x16x32_bf16 v[62:65], v[142:145], v[222:225], v[62:65]
	v_mfma_f32_16x16x32_bf16 v[58:61], v[146:149], v[222:225], v[58:61]
	v_mfma_f32_16x16x32_bf16 v[54:57], v[156:159], v[222:225], v[54:57]
	v_mfma_f32_16x16x32_bf16 v[50:53], v[160:163], v[222:225], v[50:53]
	s_add_i32 m0, s49, 0x2000
	s_nop 0
	global_load_lds_dwordx4 v90, s[30:31]
	v_mfma_f32_16x16x32_bf16 v[46:49], v[142:145], v[226:229], v[46:49]
	v_mfma_f32_16x16x32_bf16 v[42:45], v[146:149], v[226:229], v[42:45]
	v_mfma_f32_16x16x32_bf16 v[38:41], v[156:159], v[226:229], v[38:41]
	v_mfma_f32_16x16x32_bf16 v[34:37], v[160:163], v[226:229], v[34:37]
	s_add_i32 m0, s49, 0x4000
	s_nop 0
	global_load_lds_dwordx4 v92, s[30:31]
	v_mfma_f32_16x16x32_bf16 v[18:21], v[142:145], v[230:233], v[18:21]
	v_mfma_f32_16x16x32_bf16 v[22:25], v[146:149], v[230:233], v[22:25]
	v_mfma_f32_16x16x32_bf16 v[26:29], v[156:159], v[230:233], v[26:29]
	v_mfma_f32_16x16x32_bf16 v[30:33], v[160:163], v[230:233], v[30:33]
	s_add_i32 m0, s49, 0x6000
	s_nop 0
	global_load_lds_dwordx4 v94, s[30:31]
	v_mfma_f32_16x16x32_bf16 v[2:5], v[142:145], v[234:237], v[2:5]
	v_mfma_f32_16x16x32_bf16 v[6:9], v[146:149], v[234:237], v[6:9]
	v_mfma_f32_16x16x32_bf16 v[10:13], v[156:159], v[234:237], v[10:13]
	v_mfma_f32_16x16x32_bf16 v[14:17], v[160:163], v[234:237], v[14:17]
	s_add_i32 m0, s49, 0x8000
	s_nop 0
	global_load_lds_dwordx4 v96, s[30:31]
	v_cvt_pk_bf16_f32 v172, v98, v100
	v_cvt_pk_bf16_f32 v173, v102, v104
	v_cvt_pk_bf16_f32 v174, v106, v108
	v_cvt_pk_bf16_f32 v175, v110, v112
	v_cvt_pk_bf16_f32 v176, v99, v101
	v_cvt_pk_bf16_f32 v177, v103, v105
	v_cvt_pk_bf16_f32 v178, v107, v109
	v_cvt_pk_bf16_f32 v179, v111, v113
	ds_write_b128 v95, v[172:175] offset:0
	ds_write_b128 v95, v[176:179] offset:128
	v_add_u32_e32 v91, s46, v135
	v_add_u32_e32 v93, s46, v137
	ds_read_b128 v[238:241], v139 offset:19456
	ds_read_b128 v[242:245], v139 offset:21504
	ds_read_b128 v[246:249], v139 offset:23552
	ds_read_b128 v[250:253], v139 offset:25600
	ds_read_b128 v[218:221], v91 offset:0
	ds_read_b128 v[222:225], v91 offset:2048
	ds_read_b128 v[226:229], v91 offset:4096
	ds_read_b128 v[230:233], v91 offset:6144
	ds_read_b128 v[234:237], v91 offset:8192
	s_waitcnt lgkmcnt(0)
	v_mfma_f32_16x16x32_bf16 v[78:81], v[238:241], v[218:221], v[78:81]
	v_mfma_f32_16x16x32_bf16 v[74:77], v[242:245], v[218:221], v[74:77]
	v_mfma_f32_16x16x32_bf16 v[70:73], v[246:249], v[218:221], v[70:73]
	v_mfma_f32_16x16x32_bf16 v[66:69], v[250:253], v[218:221], v[66:69]
	ds_read_b128 v[218:221], v93 offset:0
	ds_read_b128 v[142:145], v141 offset:19456
	s_add_i32 s51, s51, 1
	s_and_b32 s54, s51, 7
	s_cmp_eq_u32 s54, 0
	s_cselect_b32 s44, s34, s35
	s_cselect_b32 s45, -1, 0
	v_lshl_add_u64 v[132:133], v[132:133], 0, s[44:45]
	global_load_dwordx2 v[98:99], v[132:133], off
	v_lshl_add_u64 v[180:181], v[132:133], 0, s[24:25]
	global_load_dwordx2 v[100:101], v[180:181], off
	v_mfma_f32_16x16x32_bf16 v[62:65], v[238:241], v[222:225], v[62:65]
	v_mfma_f32_16x16x32_bf16 v[58:61], v[242:245], v[222:225], v[58:61]
	v_mfma_f32_16x16x32_bf16 v[54:57], v[246:249], v[222:225], v[54:57]
	v_mfma_f32_16x16x32_bf16 v[50:53], v[250:253], v[222:225], v[50:53]
	ds_read_b128 v[222:225], v93 offset:2048
	ds_read_b128 v[146:149], v141 offset:21504
	v_lshl_add_u64 v[180:181], v[132:133], 0, s[26:27]
	global_load_dwordx2 v[102:103], v[180:181], off
	v_lshl_add_u64 v[180:181], v[132:133], 0, s[28:29]
	global_load_dwordx2 v[104:105], v[180:181], off
	v_mfma_f32_16x16x32_bf16 v[46:49], v[238:241], v[226:229], v[46:49]
	v_mfma_f32_16x16x32_bf16 v[42:45], v[242:245], v[226:229], v[42:45]
	v_mfma_f32_16x16x32_bf16 v[38:41], v[246:249], v[226:229], v[38:41]
	v_mfma_f32_16x16x32_bf16 v[34:37], v[250:253], v[226:229], v[34:37]
	ds_read_b128 v[226:229], v93 offset:4096
	ds_read_b128 v[156:159], v141 offset:23552
	v_lshl_add_u64 v[180:181], v[132:133], 0, s[36:37]
	global_load_dwordx2 v[106:107], v[180:181], off
	v_lshl_add_u64 v[180:181], v[132:133], 0, s[38:39]
	global_load_dwordx2 v[108:109], v[180:181], off
	v_mfma_f32_16x16x32_bf16 v[18:21], v[238:241], v[230:233], v[18:21]
	v_mfma_f32_16x16x32_bf16 v[22:25], v[242:245], v[230:233], v[22:25]
	v_mfma_f32_16x16x32_bf16 v[26:29], v[246:249], v[230:233], v[26:29]
	v_mfma_f32_16x16x32_bf16 v[30:33], v[250:253], v[230:233], v[30:33]
	ds_read_b128 v[230:233], v93 offset:6144
	ds_read_b128 v[160:163], v141 offset:25600
	v_lshl_add_u64 v[180:181], v[132:133], 0, s[40:41]
	global_load_dwordx2 v[110:111], v[180:181], off
	v_lshl_add_u64 v[180:181], v[132:133], 0, s[42:43]
	global_load_dwordx2 v[112:113], v[180:181], off
	v_mfma_f32_16x16x32_bf16 v[2:5], v[238:241], v[234:237], v[2:5]
	v_mfma_f32_16x16x32_bf16 v[6:9], v[242:245], v[234:237], v[6:9]
	v_mfma_f32_16x16x32_bf16 v[10:13], v[246:249], v[234:237], v[10:13]
	v_mfma_f32_16x16x32_bf16 v[14:17], v[250:253], v[234:237], v[14:17]
	ds_read_b128 v[234:237], v93 offset:8192
	s_waitcnt vmcnt(21)
	s_waitcnt lgkmcnt(0)
	s_barrier
	s_mov_b32 s49, s46
	s_mov_b32 s46, s47
	s_mov_b32 s47, s48
	s_mov_b32 s48, s49
	s_add_i32 s50, s50, 1
	s_mov_b32 s56, 13

; #define PG8_LAS __attribute__((address_space(3)))
; __device__ __forceinline__ unsigned cvtpk(float lo, float hi) { f32x2 v = {lo, hi}; bf16x2_t b = __builtin_convertvector(v, bf16x2_t); return __builtin_bit_cast(unsigned, b); }
; #define MD_GLDS_A(buf, tau) do { _Pragma("unroll") for (int i = 0; i < 5; ++i) if (amask & (1u << i)) \
;         __builtin_amdgcn_global_load_lds((const unsigned*)((const char*)HIDp + aoff[i] + (size_t)((tau) & 7) * 128), (PG8_LAS unsigned*)(MD_SA(buf) + wid * 1024 + i * 8192), 16, 0, 0); } while (0)
; __device__ __forceinline__ void moe_down_stream(PG8_LAS unsigned char* lds, int e, int cb0, int slot0, int nv, const bf16_t* HIDp, const float* Wd, bf16_t* Y, const float* slot_w, const int* slot_dst) {
;     ...
;     for (int t = 0; t < NT; t += 2) {
;         if (t + 2 < NT) MD_B_WAIT(s1, 8); else MD_B_WAIT(s1, 0);
;         MD_B_WRITE(s1, 1); __builtin_amdgcn_sched_barrier(0); MD_GLDS_A(1, t + 1); __builtin_amdgcn_sched_barrier(0);
;         if (t + 3 < NT) MD_B_ISSUE(s1, t + 3);
;         MD_COMPUTE(0);
;         MD_END(t + 3 >= NT);
;         if (t + 2 < NT) { MD_B_WAIT(s0, 8); MD_B_WRITE(s0, 0); __builtin_amdgcn_sched_barrier(0); MD_GLDS_A(0, t + 2); __builtin_amdgcn_sched_barrier(0); }
;         if (t + 4 < NT) MD_B_ISSUE(s0, t + 4);
;         MD_COMPUTE(1);
;         MD_END(t + 4 >= NT);
;         if (((t + 1) & 7) == 7) {
;             const int cb = cb0 + ((t + 1) >> 3);
; #pragma unroll
;             for (int m = 0; m < DNM; ++m) {
;                 const float w_ = lw[4 * (16 * m + fr) + wr];
; #pragma unroll
;                 for (int p = 0; p < 2; ++p) { const f32x4 v0 = acc[m][2 * p] * w_, v1 = acc[m][2 * p + 1] * w_; u32x4 w; w.x = cvtpk(v0[0], v0[1]); w.y = cvtpk(v0[2], v0[3]); w.z = cvtpk(v1[0], v1[1]); w.w = cvtpk(v1[2], v1[3]);
;                     *(PG8_LAS u32x4*)(stg + fr * 128 + (((4 * p + fq) ^ (fr & 7)) * 16)) = w; }
; #pragma unroll
;                 for (int hh = 0; hh < 2; ++hh) { const int r = (lane >> 3) + 8 * hh, cc = lane & 7; const u32x4 d = *(const PG8_LAS u32x4*)(stg + r * 128 + ((cc ^ (r & 7)) * 16)); const int dst_ = ldst[4 * (16 * m + r) + wr];
;                     if (dst_ >= 0) *(u32x4*)(Y + (size_t)dst_ * D + 128 * cb + 64 * wc + 8 * cc) = d; }
; #pragma unroll
;                 for (int n = 0; n < 4; ++n) acc[m][n] = (f32x4){0.f, 0.f, 0.f, 0.f}; } }
;     }
.Lmd_done:
	s_setprio 0
	s_branch .LBB0_789

